# radix select histogram phase: pass 0 specialised without prefix filter; passes 2-3 skip 8-key groups with no prefix match (exact); on top of score-loop pipelining
# speedup vs baseline: 1.0111x; 1.0009x over previous
; #define LAS __attribute__((address_space(3)))
; __global__ void __launch_bounds__(NWAVES * 64, 2) mega_fwd(Args args) {
;     ...
;             for (int pass = 0; pass < 4; ++pass) { const int shift = 24 - 8 * pass;
;                 LAS unsigned* qst = (LAS unsigned*)(F.lds + 40960 + (pass & 1) * 512); LAS unsigned* qstn = (LAS unsigned*)(F.lds + 40960 + ((pass & 1) ^ 1) * 512);
;                 for (int i2 = tid; i2 < 32 * HSTR; i2 += 512) hist[i2] = 0u;
;                 __syncthreads();
;                 if (pass > 0) prefix = qst[2 * r32];
;                 const int pshift = (pass == 0) ? 31 : shift + 8; const unsigned pmask = (pass == 0) ? 0u : 0xffffffffu;
; #pragma unroll
;                 for (int ti = 0; ti < 4; ++ti)
; #pragma unroll
;                     for (int e = 0; e < 32; ++e) { const unsigned k = keys[ti][e];
;                         const unsigned x = ((k >> pshift) ^ prefix) & pmask; const unsigned inc = 1u - __builtin_elementwise_min(x, 1u);
;                         if (F.wave + 8 * ti < ntiles) __hip_atomic_fetch_add(hist + r32 * HSTR + ((k >> shift) & 255u), inc, __ATOMIC_RELAXED, __HIP_MEMORY_SCOPE_WORKGROUP);
;                         if ((e & 7) == 7) __builtin_amdgcn_sched_barrier(0); }
.LBB0_667:
	s_lshl_b32 s63, s26, 3
	s_sub_i32 s62, 24, s63
	s_sub_i32 s63, 32, s63
	s_and_b64 s[76:77], s[54:55], exec
	s_cselect_b32 s63, 31, s63
	s_cmp_ge_u32 s26, 2
	s_cselect_b64 s[78:79], -1, 0
	s_lshl_b32 s92, 1, s63
	s_waitcnt lgkmcnt(0)
	v_lshlrev_b32_e32 v181, s63, v15
	s_and_b64 vcc, exec, s[54:55]
	s_cbranch_vccz .Lrx_generic
	s_and_b64 vcc, exec, s[38:39]
	s_cbranch_vccnz .Lrx_p0_g1
	v_bfe_u32 v4, v115, 24, 8
	v_bfe_u32 v5, v116, 24, 8
	v_bfe_u32 v172, v114, 24, 8
	v_bfe_u32 v173, v117, 24, 8
	v_lshl_add_u32 v4, v4, 2, v3
	v_lshl_add_u32 v5, v5, 2, v3
	v_lshl_add_u32 v172, v172, 2, v3
	v_lshl_add_u32 v173, v173, 2, v3
	ds_add_u32 v4, v232
	ds_add_u32 v5, v232
	ds_add_u32 v172, v232
	ds_add_u32 v173, v232
	v_bfe_u32 v4, v50, 24, 8
	v_bfe_u32 v5, v51, 24, 8
	v_bfe_u32 v172, v52, 24, 8
	v_bfe_u32 v173, v53, 24, 8
	v_lshl_add_u32 v4, v4, 2, v3
	v_lshl_add_u32 v5, v5, 2, v3
	v_lshl_add_u32 v172, v172, 2, v3
	v_lshl_add_u32 v173, v173, 2, v3
	ds_add_u32 v4, v232
	ds_add_u32 v5, v232
	ds_add_u32 v172, v232
	ds_add_u32 v173, v232
.Lrx_p0_g1:
	s_and_b64 vcc, exec, s[38:39]
	s_cbranch_vccnz .Lrx_p0_g2
	v_bfe_u32 v4, v42, 24, 8
	v_bfe_u32 v5, v43, 24, 8
	v_bfe_u32 v172, v44, 24, 8
	v_bfe_u32 v173, v45, 24, 8
	v_lshl_add_u32 v4, v4, 2, v3
	v_lshl_add_u32 v5, v5, 2, v3
	v_lshl_add_u32 v172, v172, 2, v3
	v_lshl_add_u32 v173, v173, 2, v3
	ds_add_u32 v4, v232
	ds_add_u32 v5, v232
	ds_add_u32 v172, v232
	ds_add_u32 v173, v232
	v_bfe_u32 v4, v46, 24, 8
	v_bfe_u32 v5, v47, 24, 8
	v_bfe_u32 v172, v48, 24, 8
	v_bfe_u32 v173, v49, 24, 8
	v_lshl_add_u32 v4, v4, 2, v3
	v_lshl_add_u32 v5, v5, 2, v3
	v_lshl_add_u32 v172, v172, 2, v3
	v_lshl_add_u32 v173, v173, 2, v3
	ds_add_u32 v4, v232
	ds_add_u32 v5, v232
	ds_add_u32 v172, v232
	ds_add_u32 v173, v232
.Lrx_p0_g2:
	s_and_b64 vcc, exec, s[38:39]
	s_cbranch_vccnz .Lrx_p0_g3
	v_bfe_u32 v4, v139, 24, 8
	v_bfe_u32 v5, v136, 24, 8
	v_bfe_u32 v172, v138, 24, 8
	v_bfe_u32 v173, v134, 24, 8
	v_lshl_add_u32 v4, v4, 2, v3
	v_lshl_add_u32 v5, v5, 2, v3
	v_lshl_add_u32 v172, v172, 2, v3
	v_lshl_add_u32 v173, v173, 2, v3
	ds_add_u32 v4, v232
	ds_add_u32 v5, v232
	ds_add_u32 v172, v232
	ds_add_u32 v173, v232
	v_bfe_u32 v4, v135, 24, 8
	v_bfe_u32 v5, v137, 24, 8
	v_bfe_u32 v172, v133, 24, 8
	v_bfe_u32 v173, v131, 24, 8
	v_lshl_add_u32 v4, v4, 2, v3
	v_lshl_add_u32 v5, v5, 2, v3
	v_lshl_add_u32 v172, v172, 2, v3
	v_lshl_add_u32 v173, v173, 2, v3
	ds_add_u32 v4, v232
	ds_add_u32 v5, v232
	ds_add_u32 v172, v232
	ds_add_u32 v173, v232
.Lrx_p0_g3:
	s_and_b64 vcc, exec, s[38:39]
	s_cbranch_vccnz .Lrx_p0_g4
	v_bfe_u32 v4, v132, 24, 8
	v_bfe_u32 v5, v127, 24, 8
	v_bfe_u32 v172, v126, 24, 8
	v_bfe_u32 v173, v129, 24, 8
	v_lshl_add_u32 v4, v4, 2, v3
	v_lshl_add_u32 v5, v5, 2, v3
	v_lshl_add_u32 v172, v172, 2, v3
	v_lshl_add_u32 v173, v173, 2, v3
	ds_add_u32 v4, v232
	ds_add_u32 v5, v232
	ds_add_u32 v172, v232
	ds_add_u32 v173, v232
	v_bfe_u32 v4, v130, 24, 8
	v_bfe_u32 v5, v128, 24, 8
	v_bfe_u32 v172, v125, 24, 8
	v_bfe_u32 v173, v62, 24, 8
	v_lshl_add_u32 v4, v4, 2, v3
	v_lshl_add_u32 v5, v5, 2, v3
	v_lshl_add_u32 v172, v172, 2, v3
	v_lshl_add_u32 v173, v173, 2, v3
	ds_add_u32 v4, v232
	ds_add_u32 v5, v232
	ds_add_u32 v172, v232
	ds_add_u32 v173, v232
.Lrx_p0_g4:
	s_and_b64 vcc, exec, s[36:37]
	s_cbranch_vccnz .Lrx_p0_g5
	v_bfe_u32 v4, v119, 24, 8
	v_bfe_u32 v5, v120, 24, 8
	v_bfe_u32 v172, v118, 24, 8
	v_bfe_u32 v173, v121, 24, 8
	v_lshl_add_u32 v4, v4, 2, v3
	v_lshl_add_u32 v5, v5, 2, v3
	v_lshl_add_u32 v172, v172, 2, v3
	v_lshl_add_u32 v173, v173, 2, v3
	ds_add_u32 v4, v232
	ds_add_u32 v5, v232
	ds_add_u32 v172, v232
	ds_add_u32 v173, v232
	v_bfe_u32 v4, v82, 24, 8
	v_bfe_u32 v5, v83, 24, 8
	v_bfe_u32 v172, v84, 24, 8
	v_bfe_u32 v173, v85, 24, 8
	v_lshl_add_u32 v4, v4, 2, v3
	v_lshl_add_u32 v5, v5, 2, v3
	v_lshl_add_u32 v172, v172, 2, v3
	v_lshl_add_u32 v173, v173, 2, v3
	ds_add_u32 v4, v232
	ds_add_u32 v5, v232
	ds_add_u32 v172, v232
	ds_add_u32 v173, v232
.Lrx_p0_g5:
	s_and_b64 vcc, exec, s[36:37]
	s_cbranch_vccnz .Lrx_p0_g6
	v_bfe_u32 v4, v74, 24, 8
	v_bfe_u32 v5, v75, 24, 8
	v_bfe_u32 v172, v76, 24, 8
	v_bfe_u32 v173, v77, 24, 8
	v_lshl_add_u32 v4, v4, 2, v3
	v_lshl_add_u32 v5, v5, 2, v3
	v_lshl_add_u32 v172, v172, 2, v3
	v_lshl_add_u32 v173, v173, 2, v3
	ds_add_u32 v4, v232
	ds_add_u32 v5, v232
	ds_add_u32 v172, v232
	ds_add_u32 v173, v232
	v_bfe_u32 v4, v78, 24, 8
	v_bfe_u32 v5, v79, 24, 8
	v_bfe_u32 v172, v80, 24, 8
	v_bfe_u32 v173, v81, 24, 8
	v_lshl_add_u32 v4, v4, 2, v3
	v_lshl_add_u32 v5, v5, 2, v3
	v_lshl_add_u32 v172, v172, 2, v3
	v_lshl_add_u32 v173, v173, 2, v3
	ds_add_u32 v4, v232
	ds_add_u32 v5, v232
	ds_add_u32 v172, v232
	ds_add_u32 v173, v232
.Lrx_p0_g6:
	s_and_b64 vcc, exec, s[36:37]
	s_cbranch_vccnz .Lrx_p0_g7
	v_bfe_u32 v4, v156, 24, 8
	v_bfe_u32 v5, v153, 24, 8
	v_bfe_u32 v172, v155, 24, 8
	v_bfe_u32 v173, v151, 24, 8
	v_lshl_add_u32 v4, v4, 2, v3
	v_lshl_add_u32 v5, v5, 2, v3
	v_lshl_add_u32 v172, v172, 2, v3
	v_lshl_add_u32 v173, v173, 2, v3
	ds_add_u32 v4, v232
	ds_add_u32 v5, v232
	ds_add_u32 v172, v232
	ds_add_u32 v173, v232
	v_bfe_u32 v4, v152, 24, 8
	v_bfe_u32 v5, v154, 24, 8
	v_bfe_u32 v172, v150, 24, 8
	v_bfe_u32 v173, v148, 24, 8
	v_lshl_add_u32 v4, v4, 2, v3
	v_lshl_add_u32 v5, v5, 2, v3
	v_lshl_add_u32 v172, v172, 2, v3
	v_lshl_add_u32 v173, v173, 2, v3
	ds_add_u32 v4, v232
	ds_add_u32 v5, v232
	ds_add_u32 v172, v232
	ds_add_u32 v173, v232
; #define LAS __attribute__((address_space(3)))
; __global__ void __launch_bounds__(NWAVES * 64, 2) mega_fwd(Args args) {
;     ...
;             for (int pass = 0; pass < 4; ++pass) { const int shift = 24 - 8 * pass;
;                 LAS unsigned* qst = (LAS unsigned*)(F.lds + 40960 + (pass & 1) * 512); LAS unsigned* qstn = (LAS unsigned*)(F.lds + 40960 + ((pass & 1) ^ 1) * 512);
;                 for (int i2 = tid; i2 < 32 * HSTR; i2 += 512) hist[i2] = 0u;
;                 __syncthreads();
;                 if (pass > 0) prefix = qst[2 * r32];
;                 const int pshift = (pass == 0) ? 31 : shift + 8; const unsigned pmask = (pass == 0) ? 0u : 0xffffffffu;
; #pragma unroll
;                 for (int ti = 0; ti < 4; ++ti)
; #pragma unroll
;                     for (int e = 0; e < 32; ++e) { const unsigned k = keys[ti][e];
;                         const unsigned x = ((k >> pshift) ^ prefix) & pmask; const unsigned inc = 1u - __builtin_elementwise_min(x, 1u);
;                         if (F.wave + 8 * ti < ntiles) __hip_atomic_fetch_add(hist + r32 * HSTR + ((k >> shift) & 255u), inc, __ATOMIC_RELAXED, __HIP_MEMORY_SCOPE_WORKGROUP);
;                         if ((e & 7) == 7) __builtin_amdgcn_sched_barrier(0); }
.Lrx_p0_g7:
	s_and_b64 vcc, exec, s[36:37]
	s_cbranch_vccnz .Lrx_p0_g8
	v_bfe_u32 v4, v149, 24, 8
	v_bfe_u32 v5, v144, 24, 8
	v_bfe_u32 v172, v143, 24, 8
	v_bfe_u32 v173, v146, 24, 8
	v_lshl_add_u32 v4, v4, 2, v3
	v_lshl_add_u32 v5, v5, 2, v3
	v_lshl_add_u32 v172, v172, 2, v3
	v_lshl_add_u32 v173, v173, 2, v3
	ds_add_u32 v4, v232
	ds_add_u32 v5, v232
	ds_add_u32 v172, v232
	ds_add_u32 v173, v232
	v_bfe_u32 v4, v147, 24, 8
	v_bfe_u32 v5, v145, 24, 8
	v_bfe_u32 v172, v63, 24, 8
	v_bfe_u32 v173, v94, 24, 8
	v_lshl_add_u32 v4, v4, 2, v3
	v_lshl_add_u32 v5, v5, 2, v3
	v_lshl_add_u32 v172, v172, 2, v3
	v_lshl_add_u32 v173, v173, 2, v3
	ds_add_u32 v4, v232
	ds_add_u32 v5, v232
	ds_add_u32 v172, v232
	ds_add_u32 v173, v232
.Lrx_p0_g8:
	s_and_b64 vcc, exec, s[34:35]
	s_cbranch_vccnz .Lrx_p0_g9
	v_bfe_u32 v4, v109, 24, 8
	v_bfe_u32 v5, v122, 24, 8
	v_bfe_u32 v172, v108, 24, 8
	v_bfe_u32 v173, v123, 24, 8
	v_lshl_add_u32 v4, v4, 2, v3
	v_lshl_add_u32 v5, v5, 2, v3
	v_lshl_add_u32 v172, v172, 2, v3
	v_lshl_add_u32 v173, v173, 2, v3
	ds_add_u32 v4, v232
	ds_add_u32 v5, v232
	ds_add_u32 v172, v232
	ds_add_u32 v173, v232
	v_bfe_u32 v4, v96, 24, 8
	v_bfe_u32 v5, v97, 24, 8
	v_bfe_u32 v172, v98, 24, 8
	v_bfe_u32 v173, v99, 24, 8
	v_lshl_add_u32 v4, v4, 2, v3
	v_lshl_add_u32 v5, v5, 2, v3
	v_lshl_add_u32 v172, v172, 2, v3
	v_lshl_add_u32 v173, v173, 2, v3
	ds_add_u32 v4, v232
	ds_add_u32 v5, v232
	ds_add_u32 v172, v232
	ds_add_u32 v173, v232
.Lrx_p0_g9:
	s_and_b64 vcc, exec, s[34:35]
	s_cbranch_vccnz .Lrx_p0_g10
	v_bfe_u32 v4, v86, 24, 8
	v_bfe_u32 v5, v87, 24, 8
	v_bfe_u32 v172, v88, 24, 8
	v_bfe_u32 v173, v89, 24, 8
	v_lshl_add_u32 v4, v4, 2, v3
	v_lshl_add_u32 v5, v5, 2, v3
	v_lshl_add_u32 v172, v172, 2, v3
	v_lshl_add_u32 v173, v173, 2, v3
	ds_add_u32 v4, v232
	ds_add_u32 v5, v232
	ds_add_u32 v172, v232
	ds_add_u32 v173, v232
	v_bfe_u32 v4, v90, 24, 8
	v_bfe_u32 v5, v91, 24, 8
	v_bfe_u32 v172, v92, 24, 8
	v_bfe_u32 v173, v93, 24, 8
	v_lshl_add_u32 v4, v4, 2, v3
	v_lshl_add_u32 v5, v5, 2, v3
	v_lshl_add_u32 v172, v172, 2, v3
	v_lshl_add_u32 v173, v173, 2, v3
	ds_add_u32 v4, v232
	ds_add_u32 v5, v232
	ds_add_u32 v172, v232
	ds_add_u32 v173, v232
.Lrx_p0_g10:
	s_and_b64 vcc, exec, s[34:35]
	s_cbranch_vccnz .Lrx_p0_g11
	v_bfe_u32 v4, v170, 24, 8
	v_bfe_u32 v5, v167, 24, 8
	v_bfe_u32 v172, v169, 24, 8
	v_bfe_u32 v173, v165, 24, 8
	v_lshl_add_u32 v4, v4, 2, v3
	v_lshl_add_u32 v5, v5, 2, v3
	v_lshl_add_u32 v172, v172, 2, v3
	v_lshl_add_u32 v173, v173, 2, v3
	ds_add_u32 v4, v232
	ds_add_u32 v5, v232
	ds_add_u32 v172, v232
	ds_add_u32 v173, v232
	v_bfe_u32 v4, v166, 24, 8
	v_bfe_u32 v5, v168, 24, 8
	v_bfe_u32 v172, v164, 24, 8
	v_bfe_u32 v173, v162, 24, 8
	v_lshl_add_u32 v4, v4, 2, v3
	v_lshl_add_u32 v5, v5, 2, v3
	v_lshl_add_u32 v172, v172, 2, v3
	v_lshl_add_u32 v173, v173, 2, v3
	ds_add_u32 v4, v232
	ds_add_u32 v5, v232
	ds_add_u32 v172, v232
	ds_add_u32 v173, v232
.Lrx_p0_g11:
	s_and_b64 vcc, exec, s[34:35]
	s_cbranch_vccnz .Lrx_p0_g12
	v_bfe_u32 v4, v163, 24, 8
	v_bfe_u32 v5, v158, 24, 8
	v_bfe_u32 v172, v157, 24, 8
	v_bfe_u32 v173, v160, 24, 8
	v_lshl_add_u32 v4, v4, 2, v3
	v_lshl_add_u32 v5, v5, 2, v3
	v_lshl_add_u32 v172, v172, 2, v3
	v_lshl_add_u32 v173, v173, 2, v3
	ds_add_u32 v4, v232
	ds_add_u32 v5, v232
	ds_add_u32 v172, v232
	ds_add_u32 v173, v232
	v_bfe_u32 v4, v161, 24, 8
	v_bfe_u32 v5, v159, 24, 8
	v_bfe_u32 v172, v95, 24, 8
	v_bfe_u32 v173, v64, 24, 8
	v_lshl_add_u32 v4, v4, 2, v3
	v_lshl_add_u32 v5, v5, 2, v3
	v_lshl_add_u32 v172, v172, 2, v3
	v_lshl_add_u32 v173, v173, 2, v3
	ds_add_u32 v4, v232
	ds_add_u32 v5, v232
	ds_add_u32 v172, v232
	ds_add_u32 v173, v232
.Lrx_p0_g12:
	s_and_b64 vcc, exec, s[30:31]
	s_cbranch_vccnz .Lrx_p0_g13
	v_bfe_u32 v4, v105, 24, 8
	v_bfe_u32 v5, v106, 24, 8
	v_bfe_u32 v172, v104, 24, 8
	v_bfe_u32 v173, v107, 24, 8
	v_lshl_add_u32 v4, v4, 2, v3
	v_lshl_add_u32 v5, v5, 2, v3
	v_lshl_add_u32 v172, v172, 2, v3
	v_lshl_add_u32 v173, v173, 2, v3
	ds_add_u32 v4, v232
	ds_add_u32 v5, v232
	ds_add_u32 v172, v232
	ds_add_u32 v173, v232
	v_bfe_u32 v4, v66, 24, 8
	v_bfe_u32 v5, v67, 24, 8
	v_bfe_u32 v172, v68, 24, 8
	v_bfe_u32 v173, v69, 24, 8
	v_lshl_add_u32 v4, v4, 2, v3
	v_lshl_add_u32 v5, v5, 2, v3
	v_lshl_add_u32 v172, v172, 2, v3
	v_lshl_add_u32 v173, v173, 2, v3
	ds_add_u32 v4, v232
	ds_add_u32 v5, v232
	ds_add_u32 v172, v232
	ds_add_u32 v173, v232
.Lrx_p0_g13:
	s_and_b64 vcc, exec, s[30:31]
	s_cbranch_vccnz .Lrx_p0_g14
	v_bfe_u32 v4, v54, 24, 8
	v_bfe_u32 v5, v55, 24, 8
	v_bfe_u32 v172, v56, 24, 8
	v_bfe_u32 v173, v57, 24, 8
	v_lshl_add_u32 v4, v4, 2, v3
	v_lshl_add_u32 v5, v5, 2, v3
	v_lshl_add_u32 v172, v172, 2, v3
	v_lshl_add_u32 v173, v173, 2, v3
	ds_add_u32 v4, v232
	ds_add_u32 v5, v232
	ds_add_u32 v172, v232
	ds_add_u32 v173, v232
	v_bfe_u32 v4, v58, 24, 8
	v_bfe_u32 v5, v59, 24, 8
	v_bfe_u32 v172, v60, 24, 8
	v_bfe_u32 v173, v61, 24, 8
	v_lshl_add_u32 v4, v4, 2, v3
	v_lshl_add_u32 v5, v5, 2, v3
	v_lshl_add_u32 v172, v172, 2, v3
	v_lshl_add_u32 v173, v173, 2, v3
	ds_add_u32 v4, v232
	ds_add_u32 v5, v232
	ds_add_u32 v172, v232
	ds_add_u32 v173, v232
.Lrx_p0_g14:
	s_and_b64 vcc, exec, s[30:31]
	s_cbranch_vccnz .Lrx_p0_g15
	v_bfe_u32 v4, v26, 24, 8
	v_bfe_u32 v5, v23, 24, 8
	v_bfe_u32 v172, v25, 24, 8
	v_bfe_u32 v173, v21, 24, 8
	v_lshl_add_u32 v4, v4, 2, v3
	v_lshl_add_u32 v5, v5, 2, v3
	v_lshl_add_u32 v172, v172, 2, v3
	v_lshl_add_u32 v173, v173, 2, v3
	ds_add_u32 v4, v232
	ds_add_u32 v5, v232
	ds_add_u32 v172, v232
	ds_add_u32 v173, v232
	v_bfe_u32 v4, v22, 24, 8
	v_bfe_u32 v5, v24, 24, 8
	v_bfe_u32 v172, v20, 24, 8
	v_bfe_u32 v173, v18, 24, 8
	v_lshl_add_u32 v4, v4, 2, v3
	v_lshl_add_u32 v5, v5, 2, v3
	v_lshl_add_u32 v172, v172, 2, v3
	v_lshl_add_u32 v173, v173, 2, v3
	ds_add_u32 v4, v232
	ds_add_u32 v5, v232
	ds_add_u32 v172, v232
	ds_add_u32 v173, v232
.Lrx_p0_g15:
	s_and_b64 vcc, exec, s[30:31]
	s_cbranch_vccnz .Lrx_p0_g16
	v_bfe_u32 v4, v19, 24, 8
	v_bfe_u32 v5, v11, 24, 8
	v_bfe_u32 v172, v9, 24, 8
	v_bfe_u32 v173, v13, 24, 8
	v_lshl_add_u32 v4, v4, 2, v3
	v_lshl_add_u32 v5, v5, 2, v3
	v_lshl_add_u32 v172, v172, 2, v3
	v_lshl_add_u32 v173, v173, 2, v3
	ds_add_u32 v4, v232
	ds_add_u32 v5, v232
	ds_add_u32 v172, v232
	ds_add_u32 v173, v232
	v_bfe_u32 v4, v12, 24, 8
	v_bfe_u32 v5, v10, 24, 8
	v_bfe_u32 v172, v8, 24, 8
	v_bfe_u32 v173, v2, 24, 8
	v_lshl_add_u32 v4, v4, 2, v3
	v_lshl_add_u32 v5, v5, 2, v3
	v_lshl_add_u32 v172, v172, 2, v3
	v_lshl_add_u32 v173, v173, 2, v3
	ds_add_u32 v4, v232
	ds_add_u32 v5, v232
	ds_add_u32 v172, v232
	ds_add_u32 v173, v232

; #define LAS __attribute__((address_space(3)))
; __global__ void __launch_bounds__(NWAVES * 64, 2) mega_fwd(Args args) {
;     ...
;             for (int pass = 0; pass < 4; ++pass) { const int shift = 24 - 8 * pass;
;                 LAS unsigned* qst = (LAS unsigned*)(F.lds + 40960 + (pass & 1) * 512); LAS unsigned* qstn = (LAS unsigned*)(F.lds + 40960 + ((pass & 1) ^ 1) * 512);
;                 for (int i2 = tid; i2 < 32 * HSTR; i2 += 512) hist[i2] = 0u;
;                 __syncthreads();
;                 if (pass > 0) prefix = qst[2 * r32];
;                 const int pshift = (pass == 0) ? 31 : shift + 8; const unsigned pmask = (pass == 0) ? 0u : 0xffffffffu;
; #pragma unroll
;                 for (int ti = 0; ti < 4; ++ti)
; #pragma unroll
;                     for (int e = 0; e < 32; ++e) { const unsigned k = keys[ti][e];
;                         const unsigned x = ((k >> pshift) ^ prefix) & pmask; const unsigned inc = 1u - __builtin_elementwise_min(x, 1u);
;                         if (F.wave + 8 * ti < ntiles) __hip_atomic_fetch_add(hist + r32 * HSTR + ((k >> shift) & 255u), inc, __ATOMIC_RELAXED, __HIP_MEMORY_SCOPE_WORKGROUP);
;                         if ((e & 7) == 7) __builtin_amdgcn_sched_barrier(0); }
.Lrx_generic:
	s_and_b64 vcc, exec, s[38:39]
	s_cbranch_vccnz .LBB0_669
	s_and_b64 vcc, exec, s[78:79]
	s_cbranch_vccz .Lrx_slow_g0
	v_xor_b32_e32 v172, v181, v115
	v_xor_b32_e32 v173, v181, v116
	v_xor_b32_e32 v174, v181, v114
	v_xor_b32_e32 v175, v181, v117
	v_xor_b32_e32 v176, v181, v50
	v_xor_b32_e32 v177, v181, v51
	v_xor_b32_e32 v178, v181, v52
	v_xor_b32_e32 v179, v181, v53
	v_min3_u32 v172, v172, v173, v174
	v_min3_u32 v175, v175, v176, v177
	v_min3_u32 v172, v172, v175, v178
	v_min_u32_e32 v172, v172, v179
	v_cmp_gt_u32_e32 vcc, s92, v172
	s_cbranch_vccz .LBB0_669
.Lrx_slow_g0:
	v_lshrrev_b32_e32 v4, s63, v115
	s_waitcnt lgkmcnt(0)
	v_cmp_eq_u32_e32 vcc, v4, v15
	s_or_b64 s[76:77], s[54:55], vcc
	v_bfe_u32 v5, v115, s62, 8
	v_cndmask_b32_e64 v4, 0, 1, s[76:77]
	v_lshl_add_u32 v5, v5, 2, v3
	ds_add_u32 v5, v4
	v_lshrrev_b32_e32 v4, s63, v116
	v_cmp_eq_u32_e32 vcc, v4, v15
	s_or_b64 s[76:77], s[54:55], vcc
	v_bfe_u32 v5, v116, s62, 8
	v_cndmask_b32_e64 v4, 0, 1, s[76:77]
	v_lshl_add_u32 v5, v5, 2, v3
	ds_add_u32 v5, v4
	v_lshrrev_b32_e32 v4, s63, v114
	v_cmp_eq_u32_e32 vcc, v4, v15
	s_or_b64 s[76:77], s[54:55], vcc
	v_bfe_u32 v5, v114, s62, 8
	v_cndmask_b32_e64 v4, 0, 1, s[76:77]
	v_lshl_add_u32 v5, v5, 2, v3
	ds_add_u32 v5, v4
	v_lshrrev_b32_e32 v4, s63, v117
	v_cmp_eq_u32_e32 vcc, v4, v15
	s_or_b64 s[76:77], s[54:55], vcc
	v_bfe_u32 v5, v117, s62, 8
	v_cndmask_b32_e64 v4, 0, 1, s[76:77]
	v_lshl_add_u32 v5, v5, 2, v3
	ds_add_u32 v5, v4
	v_lshrrev_b32_e32 v4, s63, v50
	v_cmp_eq_u32_e32 vcc, v4, v15
	s_or_b64 s[76:77], s[54:55], vcc
	v_bfe_u32 v5, v50, s62, 8
	v_cndmask_b32_e64 v4, 0, 1, s[76:77]
	v_lshl_add_u32 v5, v5, 2, v3
	ds_add_u32 v5, v4
	v_lshrrev_b32_e32 v4, s63, v51
	v_cmp_eq_u32_e32 vcc, v4, v15
	s_or_b64 s[76:77], s[54:55], vcc
	v_bfe_u32 v5, v51, s62, 8
	v_cndmask_b32_e64 v4, 0, 1, s[76:77]
	v_lshl_add_u32 v5, v5, 2, v3
	ds_add_u32 v5, v4
	v_lshrrev_b32_e32 v4, s63, v52
	v_cmp_eq_u32_e32 vcc, v4, v15
	s_or_b64 s[76:77], s[54:55], vcc
	v_bfe_u32 v5, v52, s62, 8
	v_cndmask_b32_e64 v4, 0, 1, s[76:77]
	v_lshl_add_u32 v5, v5, 2, v3
	ds_add_u32 v5, v4
	v_lshrrev_b32_e32 v4, s63, v53
	v_cmp_eq_u32_e32 vcc, v4, v15
	s_or_b64 s[76:77], s[54:55], vcc
	v_bfe_u32 v5, v53, s62, 8
	v_cndmask_b32_e64 v4, 0, 1, s[76:77]
	v_lshl_add_u32 v5, v5, 2, v3
	ds_add_u32 v5, v4
.LBB0_669:
	s_and_b64 vcc, exec, s[38:39]
	s_cbranch_vccnz .LBB0_671
	s_and_b64 vcc, exec, s[78:79]
	s_cbranch_vccz .Lrx_slow_g1
	v_xor_b32_e32 v172, v181, v42
	v_xor_b32_e32 v173, v181, v43
	v_xor_b32_e32 v174, v181, v44
	v_xor_b32_e32 v175, v181, v45
	v_xor_b32_e32 v176, v181, v46
	v_xor_b32_e32 v177, v181, v47
	v_xor_b32_e32 v178, v181, v48
	v_xor_b32_e32 v179, v181, v49
	v_min3_u32 v172, v172, v173, v174
	v_min3_u32 v175, v175, v176, v177
	v_min3_u32 v172, v172, v175, v178
	v_min_u32_e32 v172, v172, v179
	v_cmp_gt_u32_e32 vcc, s92, v172
	s_cbranch_vccz .LBB0_671
.Lrx_slow_g1:
	v_lshrrev_b32_e32 v4, s63, v42
	s_waitcnt lgkmcnt(0)
	v_cmp_eq_u32_e32 vcc, v4, v15
	s_or_b64 s[76:77], s[54:55], vcc
	v_bfe_u32 v5, v42, s62, 8
	v_cndmask_b32_e64 v4, 0, 1, s[76:77]
	v_lshl_add_u32 v5, v5, 2, v3
	ds_add_u32 v5, v4
	v_lshrrev_b32_e32 v4, s63, v43
	v_cmp_eq_u32_e32 vcc, v4, v15
	s_or_b64 s[76:77], s[54:55], vcc
	v_bfe_u32 v5, v43, s62, 8
	v_cndmask_b32_e64 v4, 0, 1, s[76:77]
	v_lshl_add_u32 v5, v5, 2, v3
	ds_add_u32 v5, v4
	v_lshrrev_b32_e32 v4, s63, v44
	v_cmp_eq_u32_e32 vcc, v4, v15
	s_or_b64 s[76:77], s[54:55], vcc
	v_bfe_u32 v5, v44, s62, 8
	v_cndmask_b32_e64 v4, 0, 1, s[76:77]
	v_lshl_add_u32 v5, v5, 2, v3
	ds_add_u32 v5, v4
	v_lshrrev_b32_e32 v4, s63, v45
	v_cmp_eq_u32_e32 vcc, v4, v15
	s_or_b64 s[76:77], s[54:55], vcc
	v_bfe_u32 v5, v45, s62, 8
	v_cndmask_b32_e64 v4, 0, 1, s[76:77]
	v_lshl_add_u32 v5, v5, 2, v3
	ds_add_u32 v5, v4
	v_lshrrev_b32_e32 v4, s63, v46
	v_cmp_eq_u32_e32 vcc, v4, v15
	s_or_b64 s[76:77], s[54:55], vcc
	v_bfe_u32 v5, v46, s62, 8
	v_cndmask_b32_e64 v4, 0, 1, s[76:77]
	v_lshl_add_u32 v5, v5, 2, v3
	ds_add_u32 v5, v4
	v_lshrrev_b32_e32 v4, s63, v47
	v_cmp_eq_u32_e32 vcc, v4, v15
	s_or_b64 s[76:77], s[54:55], vcc
	v_bfe_u32 v5, v47, s62, 8
	v_cndmask_b32_e64 v4, 0, 1, s[76:77]
	v_lshl_add_u32 v5, v5, 2, v3
	ds_add_u32 v5, v4
	v_lshrrev_b32_e32 v4, s63, v48
	v_cmp_eq_u32_e32 vcc, v4, v15
	s_or_b64 s[76:77], s[54:55], vcc
	v_bfe_u32 v5, v48, s62, 8
	v_cndmask_b32_e64 v4, 0, 1, s[76:77]
	v_lshl_add_u32 v5, v5, 2, v3
	ds_add_u32 v5, v4
	v_lshrrev_b32_e32 v4, s63, v49
	v_cmp_eq_u32_e32 vcc, v4, v15
	s_or_b64 s[76:77], s[54:55], vcc
	v_bfe_u32 v5, v49, s62, 8
	v_cndmask_b32_e64 v4, 0, 1, s[76:77]
	v_lshl_add_u32 v5, v5, 2, v3
	ds_add_u32 v5, v4
.LBB0_671:
	s_and_b64 vcc, exec, s[38:39]
	s_cbranch_vccnz .LBB0_673
	s_and_b64 vcc, exec, s[78:79]
	s_cbranch_vccz .Lrx_slow_g2
	v_xor_b32_e32 v172, v181, v139
	v_xor_b32_e32 v173, v181, v136
	v_xor_b32_e32 v174, v181, v138
	v_xor_b32_e32 v175, v181, v134
	v_xor_b32_e32 v176, v181, v135
	v_xor_b32_e32 v177, v181, v137
	v_xor_b32_e32 v178, v181, v133
	v_xor_b32_e32 v179, v181, v131
	v_min3_u32 v172, v172, v173, v174
	v_min3_u32 v175, v175, v176, v177
	v_min3_u32 v172, v172, v175, v178
	v_min_u32_e32 v172, v172, v179
	v_cmp_gt_u32_e32 vcc, s92, v172
	s_cbranch_vccz .LBB0_673
; #define LAS __attribute__((address_space(3)))
; __global__ void __launch_bounds__(NWAVES * 64, 2) mega_fwd(Args args) {
;     ...
;             for (int pass = 0; pass < 4; ++pass) { const int shift = 24 - 8 * pass;
;                 LAS unsigned* qst = (LAS unsigned*)(F.lds + 40960 + (pass & 1) * 512); LAS unsigned* qstn = (LAS unsigned*)(F.lds + 40960 + ((pass & 1) ^ 1) * 512);
;                 for (int i2 = tid; i2 < 32 * HSTR; i2 += 512) hist[i2] = 0u;
;                 __syncthreads();
;                 if (pass > 0) prefix = qst[2 * r32];
;                 const int pshift = (pass == 0) ? 31 : shift + 8; const unsigned pmask = (pass == 0) ? 0u : 0xffffffffu;
; #pragma unroll
;                 for (int ti = 0; ti < 4; ++ti)
; #pragma unroll
;                     for (int e = 0; e < 32; ++e) { const unsigned k = keys[ti][e];
;                         const unsigned x = ((k >> pshift) ^ prefix) & pmask; const unsigned inc = 1u - __builtin_elementwise_min(x, 1u);
;                         if (F.wave + 8 * ti < ntiles) __hip_atomic_fetch_add(hist + r32 * HSTR + ((k >> shift) & 255u), inc, __ATOMIC_RELAXED, __HIP_MEMORY_SCOPE_WORKGROUP);
;                         if ((e & 7) == 7) __builtin_amdgcn_sched_barrier(0); }
.Lrx_slow_g2:
	v_lshrrev_b32_e32 v4, s63, v139
	s_waitcnt lgkmcnt(0)
	v_cmp_eq_u32_e32 vcc, v4, v15
	s_or_b64 s[76:77], s[54:55], vcc
	v_bfe_u32 v5, v139, s62, 8
	v_cndmask_b32_e64 v4, 0, 1, s[76:77]
	v_lshl_add_u32 v5, v5, 2, v3
	ds_add_u32 v5, v4
	v_lshrrev_b32_e32 v4, s63, v136
	v_cmp_eq_u32_e32 vcc, v4, v15
	s_or_b64 s[76:77], s[54:55], vcc
	v_bfe_u32 v5, v136, s62, 8
	v_cndmask_b32_e64 v4, 0, 1, s[76:77]
	v_lshl_add_u32 v5, v5, 2, v3
	ds_add_u32 v5, v4
	v_lshrrev_b32_e32 v4, s63, v138
	v_cmp_eq_u32_e32 vcc, v4, v15
	s_or_b64 s[76:77], s[54:55], vcc
	v_bfe_u32 v5, v138, s62, 8
	v_cndmask_b32_e64 v4, 0, 1, s[76:77]
	v_lshl_add_u32 v5, v5, 2, v3
	ds_add_u32 v5, v4
	v_lshrrev_b32_e32 v4, s63, v134
	v_cmp_eq_u32_e32 vcc, v4, v15
	s_or_b64 s[76:77], s[54:55], vcc
	v_bfe_u32 v5, v134, s62, 8
	v_cndmask_b32_e64 v4, 0, 1, s[76:77]
	v_lshl_add_u32 v5, v5, 2, v3
	ds_add_u32 v5, v4
	v_lshrrev_b32_e32 v4, s63, v135
	v_cmp_eq_u32_e32 vcc, v4, v15
	s_or_b64 s[76:77], s[54:55], vcc
	v_bfe_u32 v5, v135, s62, 8
	v_cndmask_b32_e64 v4, 0, 1, s[76:77]
	v_lshl_add_u32 v5, v5, 2, v3
	ds_add_u32 v5, v4
	v_lshrrev_b32_e32 v4, s63, v137
	v_cmp_eq_u32_e32 vcc, v4, v15
	s_or_b64 s[76:77], s[54:55], vcc
	v_bfe_u32 v5, v137, s62, 8
	v_cndmask_b32_e64 v4, 0, 1, s[76:77]
	v_lshl_add_u32 v5, v5, 2, v3
	ds_add_u32 v5, v4
	v_lshrrev_b32_e32 v4, s63, v133
	v_cmp_eq_u32_e32 vcc, v4, v15
	s_or_b64 s[76:77], s[54:55], vcc
	v_bfe_u32 v5, v133, s62, 8
	v_cndmask_b32_e64 v4, 0, 1, s[76:77]
	v_lshl_add_u32 v5, v5, 2, v3
	ds_add_u32 v5, v4
	v_lshrrev_b32_e32 v4, s63, v131
	v_cmp_eq_u32_e32 vcc, v4, v15
	s_or_b64 s[76:77], s[54:55], vcc
	v_bfe_u32 v5, v131, s62, 8
	v_cndmask_b32_e64 v4, 0, 1, s[76:77]
	v_lshl_add_u32 v5, v5, 2, v3
	ds_add_u32 v5, v4
.LBB0_673:
	s_and_b64 vcc, exec, s[38:39]
	s_cbranch_vccnz .LBB0_675
	s_and_b64 vcc, exec, s[78:79]
	s_cbranch_vccz .Lrx_slow_g3
	v_xor_b32_e32 v172, v181, v132
	v_xor_b32_e32 v173, v181, v127
	v_xor_b32_e32 v174, v181, v126
	v_xor_b32_e32 v175, v181, v129
	v_xor_b32_e32 v176, v181, v130
	v_xor_b32_e32 v177, v181, v128
	v_xor_b32_e32 v178, v181, v125
	v_xor_b32_e32 v179, v181, v62
	v_min3_u32 v172, v172, v173, v174
	v_min3_u32 v175, v175, v176, v177
	v_min3_u32 v172, v172, v175, v178
	v_min_u32_e32 v172, v172, v179
	v_cmp_gt_u32_e32 vcc, s92, v172
	s_cbranch_vccz .LBB0_675
.Lrx_slow_g3:
	v_lshrrev_b32_e32 v4, s63, v132
	s_waitcnt lgkmcnt(0)
	v_cmp_eq_u32_e32 vcc, v4, v15
	s_or_b64 s[76:77], s[54:55], vcc
	v_bfe_u32 v5, v132, s62, 8
	v_cndmask_b32_e64 v4, 0, 1, s[76:77]
	v_lshl_add_u32 v5, v5, 2, v3
	ds_add_u32 v5, v4
	v_lshrrev_b32_e32 v4, s63, v127
	v_cmp_eq_u32_e32 vcc, v4, v15
	s_or_b64 s[76:77], s[54:55], vcc
	v_bfe_u32 v5, v127, s62, 8
	v_cndmask_b32_e64 v4, 0, 1, s[76:77]
	v_lshl_add_u32 v5, v5, 2, v3
	ds_add_u32 v5, v4
	v_lshrrev_b32_e32 v4, s63, v126
	v_cmp_eq_u32_e32 vcc, v4, v15
	s_or_b64 s[76:77], s[54:55], vcc
	v_bfe_u32 v5, v126, s62, 8
	v_cndmask_b32_e64 v4, 0, 1, s[76:77]
	v_lshl_add_u32 v5, v5, 2, v3
	ds_add_u32 v5, v4
	v_lshrrev_b32_e32 v4, s63, v129
	v_cmp_eq_u32_e32 vcc, v4, v15
	s_or_b64 s[76:77], s[54:55], vcc
	v_bfe_u32 v5, v129, s62, 8
	v_cndmask_b32_e64 v4, 0, 1, s[76:77]
	v_lshl_add_u32 v5, v5, 2, v3
	ds_add_u32 v5, v4
	v_lshrrev_b32_e32 v4, s63, v130
	v_cmp_eq_u32_e32 vcc, v4, v15
	s_or_b64 s[76:77], s[54:55], vcc
	v_bfe_u32 v5, v130, s62, 8
	v_cndmask_b32_e64 v4, 0, 1, s[76:77]
	v_lshl_add_u32 v5, v5, 2, v3
	ds_add_u32 v5, v4
	v_lshrrev_b32_e32 v4, s63, v128
	v_cmp_eq_u32_e32 vcc, v4, v15
	s_or_b64 s[76:77], s[54:55], vcc
	v_bfe_u32 v5, v128, s62, 8
	v_cndmask_b32_e64 v4, 0, 1, s[76:77]
	v_lshl_add_u32 v5, v5, 2, v3
	ds_add_u32 v5, v4
	v_lshrrev_b32_e32 v4, s63, v125
	v_cmp_eq_u32_e32 vcc, v4, v15
	s_or_b64 s[76:77], s[54:55], vcc
	v_bfe_u32 v5, v125, s62, 8
	v_cndmask_b32_e64 v4, 0, 1, s[76:77]
	v_lshl_add_u32 v5, v5, 2, v3
	ds_add_u32 v5, v4
	v_lshrrev_b32_e32 v4, s63, v62
	v_cmp_eq_u32_e32 vcc, v4, v15
	s_or_b64 s[76:77], s[54:55], vcc
	v_bfe_u32 v5, v62, s62, 8
	v_cndmask_b32_e64 v4, 0, 1, s[76:77]
	v_lshl_add_u32 v5, v5, 2, v3
	ds_add_u32 v5, v4
.LBB0_675:
	s_and_b64 vcc, exec, s[36:37]
	s_cbranch_vccnz .LBB0_677
	s_and_b64 vcc, exec, s[78:79]
	s_cbranch_vccz .Lrx_slow_g4
	v_xor_b32_e32 v172, v181, v119
	v_xor_b32_e32 v173, v181, v120
	v_xor_b32_e32 v174, v181, v118
	v_xor_b32_e32 v175, v181, v121
	v_xor_b32_e32 v176, v181, v82
	v_xor_b32_e32 v177, v181, v83
	v_xor_b32_e32 v178, v181, v84
	v_xor_b32_e32 v179, v181, v85
	v_min3_u32 v172, v172, v173, v174
	v_min3_u32 v175, v175, v176, v177
	v_min3_u32 v172, v172, v175, v178
	v_min_u32_e32 v172, v172, v179
	v_cmp_gt_u32_e32 vcc, s92, v172
	s_cbranch_vccz .LBB0_677
.Lrx_slow_g4:
	v_lshrrev_b32_e32 v4, s63, v119
	s_waitcnt lgkmcnt(0)
	v_cmp_eq_u32_e32 vcc, v4, v15
	s_or_b64 s[76:77], s[54:55], vcc
	v_bfe_u32 v5, v119, s62, 8
	v_cndmask_b32_e64 v4, 0, 1, s[76:77]
	v_lshl_add_u32 v5, v5, 2, v3
	ds_add_u32 v5, v4
	v_lshrrev_b32_e32 v4, s63, v120
	v_cmp_eq_u32_e32 vcc, v4, v15
	s_or_b64 s[76:77], s[54:55], vcc
	v_bfe_u32 v5, v120, s62, 8
	v_cndmask_b32_e64 v4, 0, 1, s[76:77]
	v_lshl_add_u32 v5, v5, 2, v3
	ds_add_u32 v5, v4
	v_lshrrev_b32_e32 v4, s63, v118
	v_cmp_eq_u32_e32 vcc, v4, v15
	s_or_b64 s[76:77], s[54:55], vcc
	v_bfe_u32 v5, v118, s62, 8
	v_cndmask_b32_e64 v4, 0, 1, s[76:77]
	v_lshl_add_u32 v5, v5, 2, v3
	ds_add_u32 v5, v4
	v_lshrrev_b32_e32 v4, s63, v121
	v_cmp_eq_u32_e32 vcc, v4, v15
	s_or_b64 s[76:77], s[54:55], vcc
	v_bfe_u32 v5, v121, s62, 8
	v_cndmask_b32_e64 v4, 0, 1, s[76:77]
	v_lshl_add_u32 v5, v5, 2, v3
	ds_add_u32 v5, v4
	v_lshrrev_b32_e32 v4, s63, v82
	v_cmp_eq_u32_e32 vcc, v4, v15
	s_or_b64 s[76:77], s[54:55], vcc
	v_bfe_u32 v5, v82, s62, 8
	v_cndmask_b32_e64 v4, 0, 1, s[76:77]
	v_lshl_add_u32 v5, v5, 2, v3
	ds_add_u32 v5, v4
	v_lshrrev_b32_e32 v4, s63, v83
	v_cmp_eq_u32_e32 vcc, v4, v15
	s_or_b64 s[76:77], s[54:55], vcc
	v_bfe_u32 v5, v83, s62, 8
	v_cndmask_b32_e64 v4, 0, 1, s[76:77]
	v_lshl_add_u32 v5, v5, 2, v3
	ds_add_u32 v5, v4
	v_lshrrev_b32_e32 v4, s63, v84
	v_cmp_eq_u32_e32 vcc, v4, v15
	s_or_b64 s[76:77], s[54:55], vcc
	v_bfe_u32 v5, v84, s62, 8
	v_cndmask_b32_e64 v4, 0, 1, s[76:77]
	v_lshl_add_u32 v5, v5, 2, v3
	ds_add_u32 v5, v4
	v_lshrrev_b32_e32 v4, s63, v85
	v_cmp_eq_u32_e32 vcc, v4, v15
	s_or_b64 s[76:77], s[54:55], vcc
	v_bfe_u32 v5, v85, s62, 8
	v_cndmask_b32_e64 v4, 0, 1, s[76:77]
	v_lshl_add_u32 v5, v5, 2, v3
	ds_add_u32 v5, v4
; #define LAS __attribute__((address_space(3)))
; __global__ void __launch_bounds__(NWAVES * 64, 2) mega_fwd(Args args) {
;     ...
;             for (int pass = 0; pass < 4; ++pass) { const int shift = 24 - 8 * pass;
;                 LAS unsigned* qst = (LAS unsigned*)(F.lds + 40960 + (pass & 1) * 512); LAS unsigned* qstn = (LAS unsigned*)(F.lds + 40960 + ((pass & 1) ^ 1) * 512);
;                 for (int i2 = tid; i2 < 32 * HSTR; i2 += 512) hist[i2] = 0u;
;                 __syncthreads();
;                 if (pass > 0) prefix = qst[2 * r32];
;                 const int pshift = (pass == 0) ? 31 : shift + 8; const unsigned pmask = (pass == 0) ? 0u : 0xffffffffu;
; #pragma unroll
;                 for (int ti = 0; ti < 4; ++ti)
; #pragma unroll
;                     for (int e = 0; e < 32; ++e) { const unsigned k = keys[ti][e];
;                         const unsigned x = ((k >> pshift) ^ prefix) & pmask; const unsigned inc = 1u - __builtin_elementwise_min(x, 1u);
;                         if (F.wave + 8 * ti < ntiles) __hip_atomic_fetch_add(hist + r32 * HSTR + ((k >> shift) & 255u), inc, __ATOMIC_RELAXED, __HIP_MEMORY_SCOPE_WORKGROUP);
;                         if ((e & 7) == 7) __builtin_amdgcn_sched_barrier(0); }
.LBB0_677:
	s_and_b64 vcc, exec, s[36:37]
	s_cbranch_vccnz .LBB0_679
	s_and_b64 vcc, exec, s[78:79]
	s_cbranch_vccz .Lrx_slow_g5
	v_xor_b32_e32 v172, v181, v74
	v_xor_b32_e32 v173, v181, v75
	v_xor_b32_e32 v174, v181, v76
	v_xor_b32_e32 v175, v181, v77
	v_xor_b32_e32 v176, v181, v78
	v_xor_b32_e32 v177, v181, v79
	v_xor_b32_e32 v178, v181, v80
	v_xor_b32_e32 v179, v181, v81
	v_min3_u32 v172, v172, v173, v174
	v_min3_u32 v175, v175, v176, v177
	v_min3_u32 v172, v172, v175, v178
	v_min_u32_e32 v172, v172, v179
	v_cmp_gt_u32_e32 vcc, s92, v172
	s_cbranch_vccz .LBB0_679
.Lrx_slow_g5:
	v_lshrrev_b32_e32 v4, s63, v74
	s_waitcnt lgkmcnt(0)
	v_cmp_eq_u32_e32 vcc, v4, v15
	s_or_b64 s[76:77], s[54:55], vcc
	v_bfe_u32 v5, v74, s62, 8
	v_cndmask_b32_e64 v4, 0, 1, s[76:77]
	v_lshl_add_u32 v5, v5, 2, v3
	ds_add_u32 v5, v4
	v_lshrrev_b32_e32 v4, s63, v75
	v_cmp_eq_u32_e32 vcc, v4, v15
	s_or_b64 s[76:77], s[54:55], vcc
	v_bfe_u32 v5, v75, s62, 8
	v_cndmask_b32_e64 v4, 0, 1, s[76:77]
	v_lshl_add_u32 v5, v5, 2, v3
	ds_add_u32 v5, v4
	v_lshrrev_b32_e32 v4, s63, v76
	v_cmp_eq_u32_e32 vcc, v4, v15
	s_or_b64 s[76:77], s[54:55], vcc
	v_bfe_u32 v5, v76, s62, 8
	v_cndmask_b32_e64 v4, 0, 1, s[76:77]
	v_lshl_add_u32 v5, v5, 2, v3
	ds_add_u32 v5, v4
	v_lshrrev_b32_e32 v4, s63, v77
	v_cmp_eq_u32_e32 vcc, v4, v15
	s_or_b64 s[76:77], s[54:55], vcc
	v_bfe_u32 v5, v77, s62, 8
	v_cndmask_b32_e64 v4, 0, 1, s[76:77]
	v_lshl_add_u32 v5, v5, 2, v3
	ds_add_u32 v5, v4
	v_lshrrev_b32_e32 v4, s63, v78
	v_cmp_eq_u32_e32 vcc, v4, v15
	s_or_b64 s[76:77], s[54:55], vcc
	v_bfe_u32 v5, v78, s62, 8
	v_cndmask_b32_e64 v4, 0, 1, s[76:77]
	v_lshl_add_u32 v5, v5, 2, v3
	ds_add_u32 v5, v4
	v_lshrrev_b32_e32 v4, s63, v79
	v_cmp_eq_u32_e32 vcc, v4, v15
	s_or_b64 s[76:77], s[54:55], vcc
	v_bfe_u32 v5, v79, s62, 8
	v_cndmask_b32_e64 v4, 0, 1, s[76:77]
	v_lshl_add_u32 v5, v5, 2, v3
	ds_add_u32 v5, v4
	v_lshrrev_b32_e32 v4, s63, v80
	v_cmp_eq_u32_e32 vcc, v4, v15
	s_or_b64 s[76:77], s[54:55], vcc
	v_bfe_u32 v5, v80, s62, 8
	v_cndmask_b32_e64 v4, 0, 1, s[76:77]
	v_lshl_add_u32 v5, v5, 2, v3
	ds_add_u32 v5, v4
	v_lshrrev_b32_e32 v4, s63, v81
	v_cmp_eq_u32_e32 vcc, v4, v15
	s_or_b64 s[76:77], s[54:55], vcc
	v_bfe_u32 v5, v81, s62, 8
	v_cndmask_b32_e64 v4, 0, 1, s[76:77]
	v_lshl_add_u32 v5, v5, 2, v3
	ds_add_u32 v5, v4
.LBB0_679:
	s_and_b64 vcc, exec, s[36:37]
	s_cbranch_vccnz .LBB0_681
	s_and_b64 vcc, exec, s[78:79]
	s_cbranch_vccz .Lrx_slow_g6
	v_xor_b32_e32 v172, v181, v156
	v_xor_b32_e32 v173, v181, v153
	v_xor_b32_e32 v174, v181, v155
	v_xor_b32_e32 v175, v181, v151
	v_xor_b32_e32 v176, v181, v152
	v_xor_b32_e32 v177, v181, v154
	v_xor_b32_e32 v178, v181, v150
	v_xor_b32_e32 v179, v181, v148
	v_min3_u32 v172, v172, v173, v174
	v_min3_u32 v175, v175, v176, v177
	v_min3_u32 v172, v172, v175, v178
	v_min_u32_e32 v172, v172, v179
	v_cmp_gt_u32_e32 vcc, s92, v172
	s_cbranch_vccz .LBB0_681
.Lrx_slow_g6:
	v_lshrrev_b32_e32 v4, s63, v156
	s_waitcnt lgkmcnt(0)
	v_cmp_eq_u32_e32 vcc, v4, v15
	s_or_b64 s[76:77], s[54:55], vcc
	v_bfe_u32 v5, v156, s62, 8
	v_cndmask_b32_e64 v4, 0, 1, s[76:77]
	v_lshl_add_u32 v5, v5, 2, v3
	ds_add_u32 v5, v4
	v_lshrrev_b32_e32 v4, s63, v153
	v_cmp_eq_u32_e32 vcc, v4, v15
	s_or_b64 s[76:77], s[54:55], vcc
	v_bfe_u32 v5, v153, s62, 8
	v_cndmask_b32_e64 v4, 0, 1, s[76:77]
	v_lshl_add_u32 v5, v5, 2, v3
	ds_add_u32 v5, v4
	v_lshrrev_b32_e32 v4, s63, v155
	v_cmp_eq_u32_e32 vcc, v4, v15
	s_or_b64 s[76:77], s[54:55], vcc
	v_bfe_u32 v5, v155, s62, 8
	v_cndmask_b32_e64 v4, 0, 1, s[76:77]
	v_lshl_add_u32 v5, v5, 2, v3
	ds_add_u32 v5, v4
	v_lshrrev_b32_e32 v4, s63, v151
	v_cmp_eq_u32_e32 vcc, v4, v15
	s_or_b64 s[76:77], s[54:55], vcc
	v_bfe_u32 v5, v151, s62, 8
	v_cndmask_b32_e64 v4, 0, 1, s[76:77]
	v_lshl_add_u32 v5, v5, 2, v3
	ds_add_u32 v5, v4
	v_lshrrev_b32_e32 v4, s63, v152
	v_cmp_eq_u32_e32 vcc, v4, v15
	s_or_b64 s[76:77], s[54:55], vcc
	v_bfe_u32 v5, v152, s62, 8
	v_cndmask_b32_e64 v4, 0, 1, s[76:77]
	v_lshl_add_u32 v5, v5, 2, v3
	ds_add_u32 v5, v4
	v_lshrrev_b32_e32 v4, s63, v154
	v_cmp_eq_u32_e32 vcc, v4, v15
	s_or_b64 s[76:77], s[54:55], vcc
	v_bfe_u32 v5, v154, s62, 8
	v_cndmask_b32_e64 v4, 0, 1, s[76:77]
	v_lshl_add_u32 v5, v5, 2, v3
	ds_add_u32 v5, v4
	v_lshrrev_b32_e32 v4, s63, v150
	v_cmp_eq_u32_e32 vcc, v4, v15
	s_or_b64 s[76:77], s[54:55], vcc
	v_bfe_u32 v5, v150, s62, 8
	v_cndmask_b32_e64 v4, 0, 1, s[76:77]
	v_lshl_add_u32 v5, v5, 2, v3
	ds_add_u32 v5, v4
	v_lshrrev_b32_e32 v4, s63, v148
	v_cmp_eq_u32_e32 vcc, v4, v15
	s_or_b64 s[76:77], s[54:55], vcc
	v_bfe_u32 v5, v148, s62, 8
	v_cndmask_b32_e64 v4, 0, 1, s[76:77]
	v_lshl_add_u32 v5, v5, 2, v3
	ds_add_u32 v5, v4
.LBB0_681:
	s_and_b64 vcc, exec, s[36:37]
	s_cbranch_vccnz .LBB0_683
	s_and_b64 vcc, exec, s[78:79]
	s_cbranch_vccz .Lrx_slow_g7
	v_xor_b32_e32 v172, v181, v149
	v_xor_b32_e32 v173, v181, v144
	v_xor_b32_e32 v174, v181, v143
	v_xor_b32_e32 v175, v181, v146
	v_xor_b32_e32 v176, v181, v147
	v_xor_b32_e32 v177, v181, v145
	v_xor_b32_e32 v178, v181, v63
	v_xor_b32_e32 v179, v181, v94
	v_min3_u32 v172, v172, v173, v174
	v_min3_u32 v175, v175, v176, v177
	v_min3_u32 v172, v172, v175, v178
	v_min_u32_e32 v172, v172, v179
	v_cmp_gt_u32_e32 vcc, s92, v172
	s_cbranch_vccz .LBB0_683
; #define LAS __attribute__((address_space(3)))
; __global__ void __launch_bounds__(NWAVES * 64, 2) mega_fwd(Args args) {
;     ...
;             for (int pass = 0; pass < 4; ++pass) { const int shift = 24 - 8 * pass;
;                 LAS unsigned* qst = (LAS unsigned*)(F.lds + 40960 + (pass & 1) * 512); LAS unsigned* qstn = (LAS unsigned*)(F.lds + 40960 + ((pass & 1) ^ 1) * 512);
;                 for (int i2 = tid; i2 < 32 * HSTR; i2 += 512) hist[i2] = 0u;
;                 __syncthreads();
;                 if (pass > 0) prefix = qst[2 * r32];
;                 const int pshift = (pass == 0) ? 31 : shift + 8; const unsigned pmask = (pass == 0) ? 0u : 0xffffffffu;
; #pragma unroll
;                 for (int ti = 0; ti < 4; ++ti)
; #pragma unroll
;                     for (int e = 0; e < 32; ++e) { const unsigned k = keys[ti][e];
;                         const unsigned x = ((k >> pshift) ^ prefix) & pmask; const unsigned inc = 1u - __builtin_elementwise_min(x, 1u);
;                         if (F.wave + 8 * ti < ntiles) __hip_atomic_fetch_add(hist + r32 * HSTR + ((k >> shift) & 255u), inc, __ATOMIC_RELAXED, __HIP_MEMORY_SCOPE_WORKGROUP);
;                         if ((e & 7) == 7) __builtin_amdgcn_sched_barrier(0); }
.Lrx_slow_g7:
	v_lshrrev_b32_e32 v4, s63, v149
	s_waitcnt lgkmcnt(0)
	v_cmp_eq_u32_e32 vcc, v4, v15
	s_or_b64 s[76:77], s[54:55], vcc
	v_bfe_u32 v5, v149, s62, 8
	v_cndmask_b32_e64 v4, 0, 1, s[76:77]
	v_lshl_add_u32 v5, v5, 2, v3
	ds_add_u32 v5, v4
	v_lshrrev_b32_e32 v4, s63, v144
	v_cmp_eq_u32_e32 vcc, v4, v15
	s_or_b64 s[76:77], s[54:55], vcc
	v_bfe_u32 v5, v144, s62, 8
	v_cndmask_b32_e64 v4, 0, 1, s[76:77]
	v_lshl_add_u32 v5, v5, 2, v3
	ds_add_u32 v5, v4
	v_lshrrev_b32_e32 v4, s63, v143
	v_cmp_eq_u32_e32 vcc, v4, v15
	s_or_b64 s[76:77], s[54:55], vcc
	v_bfe_u32 v5, v143, s62, 8
	v_cndmask_b32_e64 v4, 0, 1, s[76:77]
	v_lshl_add_u32 v5, v5, 2, v3
	ds_add_u32 v5, v4
	v_lshrrev_b32_e32 v4, s63, v146
	v_cmp_eq_u32_e32 vcc, v4, v15
	s_or_b64 s[76:77], s[54:55], vcc
	v_bfe_u32 v5, v146, s62, 8
	v_cndmask_b32_e64 v4, 0, 1, s[76:77]
	v_lshl_add_u32 v5, v5, 2, v3
	ds_add_u32 v5, v4
	v_lshrrev_b32_e32 v4, s63, v147
	v_cmp_eq_u32_e32 vcc, v4, v15
	s_or_b64 s[76:77], s[54:55], vcc
	v_bfe_u32 v5, v147, s62, 8
	v_cndmask_b32_e64 v4, 0, 1, s[76:77]
	v_lshl_add_u32 v5, v5, 2, v3
	ds_add_u32 v5, v4
	v_lshrrev_b32_e32 v4, s63, v145
	v_cmp_eq_u32_e32 vcc, v4, v15
	s_or_b64 s[76:77], s[54:55], vcc
	v_bfe_u32 v5, v145, s62, 8
	v_cndmask_b32_e64 v4, 0, 1, s[76:77]
	v_lshl_add_u32 v5, v5, 2, v3
	ds_add_u32 v5, v4
	v_lshrrev_b32_e32 v4, s63, v63
	v_cmp_eq_u32_e32 vcc, v4, v15
	s_or_b64 s[76:77], s[54:55], vcc
	v_bfe_u32 v5, v63, s62, 8
	v_cndmask_b32_e64 v4, 0, 1, s[76:77]
	v_lshl_add_u32 v5, v5, 2, v3
	ds_add_u32 v5, v4
	v_lshrrev_b32_e32 v4, s63, v94
	v_cmp_eq_u32_e32 vcc, v4, v15
	s_or_b64 s[76:77], s[54:55], vcc
	v_bfe_u32 v5, v94, s62, 8
	v_cndmask_b32_e64 v4, 0, 1, s[76:77]
	v_lshl_add_u32 v5, v5, 2, v3
	ds_add_u32 v5, v4
.LBB0_683:
	s_and_b64 vcc, exec, s[34:35]
	s_cbranch_vccnz .LBB0_685
	s_and_b64 vcc, exec, s[78:79]
	s_cbranch_vccz .Lrx_slow_g8
	v_xor_b32_e32 v172, v181, v109
	v_xor_b32_e32 v173, v181, v122
	v_xor_b32_e32 v174, v181, v108
	v_xor_b32_e32 v175, v181, v123
	v_xor_b32_e32 v176, v181, v96
	v_xor_b32_e32 v177, v181, v97
	v_xor_b32_e32 v178, v181, v98
	v_xor_b32_e32 v179, v181, v99
	v_min3_u32 v172, v172, v173, v174
	v_min3_u32 v175, v175, v176, v177
	v_min3_u32 v172, v172, v175, v178
	v_min_u32_e32 v172, v172, v179
	v_cmp_gt_u32_e32 vcc, s92, v172
	s_cbranch_vccz .LBB0_685
.Lrx_slow_g8:
	v_lshrrev_b32_e32 v4, s63, v109
	s_waitcnt lgkmcnt(0)
	v_cmp_eq_u32_e32 vcc, v4, v15
	s_or_b64 s[76:77], s[54:55], vcc
	v_bfe_u32 v5, v109, s62, 8
	v_cndmask_b32_e64 v4, 0, 1, s[76:77]
	v_lshl_add_u32 v5, v5, 2, v3
	ds_add_u32 v5, v4
	v_lshrrev_b32_e32 v4, s63, v122
	v_cmp_eq_u32_e32 vcc, v4, v15
	s_or_b64 s[76:77], s[54:55], vcc
	v_bfe_u32 v5, v122, s62, 8
	v_cndmask_b32_e64 v4, 0, 1, s[76:77]
	v_lshl_add_u32 v5, v5, 2, v3
	ds_add_u32 v5, v4
	v_lshrrev_b32_e32 v4, s63, v108
	v_cmp_eq_u32_e32 vcc, v4, v15
	s_or_b64 s[76:77], s[54:55], vcc
	v_bfe_u32 v5, v108, s62, 8
	v_cndmask_b32_e64 v4, 0, 1, s[76:77]
	v_lshl_add_u32 v5, v5, 2, v3
	ds_add_u32 v5, v4
	v_lshrrev_b32_e32 v4, s63, v123
	v_cmp_eq_u32_e32 vcc, v4, v15
	s_or_b64 s[76:77], s[54:55], vcc
	v_bfe_u32 v5, v123, s62, 8
	v_cndmask_b32_e64 v4, 0, 1, s[76:77]
	v_lshl_add_u32 v5, v5, 2, v3
	ds_add_u32 v5, v4
	v_lshrrev_b32_e32 v4, s63, v96
	v_cmp_eq_u32_e32 vcc, v4, v15
	s_or_b64 s[76:77], s[54:55], vcc
	v_bfe_u32 v5, v96, s62, 8
	v_cndmask_b32_e64 v4, 0, 1, s[76:77]
	v_lshl_add_u32 v5, v5, 2, v3
	ds_add_u32 v5, v4
	v_lshrrev_b32_e32 v4, s63, v97
	v_cmp_eq_u32_e32 vcc, v4, v15
	s_or_b64 s[76:77], s[54:55], vcc
	v_bfe_u32 v5, v97, s62, 8
	v_cndmask_b32_e64 v4, 0, 1, s[76:77]
	v_lshl_add_u32 v5, v5, 2, v3
	ds_add_u32 v5, v4
	v_lshrrev_b32_e32 v4, s63, v98
	v_cmp_eq_u32_e32 vcc, v4, v15
	s_or_b64 s[76:77], s[54:55], vcc
	v_bfe_u32 v5, v98, s62, 8
	v_cndmask_b32_e64 v4, 0, 1, s[76:77]
	v_lshl_add_u32 v5, v5, 2, v3
	ds_add_u32 v5, v4
	v_lshrrev_b32_e32 v4, s63, v99
	v_cmp_eq_u32_e32 vcc, v4, v15
	s_or_b64 s[76:77], s[54:55], vcc
	v_bfe_u32 v5, v99, s62, 8
	v_cndmask_b32_e64 v4, 0, 1, s[76:77]
	v_lshl_add_u32 v5, v5, 2, v3
	ds_add_u32 v5, v4
.LBB0_685:
	s_and_b64 vcc, exec, s[34:35]
	s_cbranch_vccnz .LBB0_687
	s_and_b64 vcc, exec, s[78:79]
	s_cbranch_vccz .Lrx_slow_g9
	v_xor_b32_e32 v172, v181, v86
	v_xor_b32_e32 v173, v181, v87
	v_xor_b32_e32 v174, v181, v88
	v_xor_b32_e32 v175, v181, v89
	v_xor_b32_e32 v176, v181, v90
	v_xor_b32_e32 v177, v181, v91
	v_xor_b32_e32 v178, v181, v92
	v_xor_b32_e32 v179, v181, v93
	v_min3_u32 v172, v172, v173, v174
	v_min3_u32 v175, v175, v176, v177
	v_min3_u32 v172, v172, v175, v178
	v_min_u32_e32 v172, v172, v179
	v_cmp_gt_u32_e32 vcc, s92, v172
	s_cbranch_vccz .LBB0_687
.Lrx_slow_g9:
	v_lshrrev_b32_e32 v4, s63, v86
	s_waitcnt lgkmcnt(0)
	v_cmp_eq_u32_e32 vcc, v4, v15
	s_or_b64 s[76:77], s[54:55], vcc
	v_bfe_u32 v5, v86, s62, 8
	v_cndmask_b32_e64 v4, 0, 1, s[76:77]
	v_lshl_add_u32 v5, v5, 2, v3
	ds_add_u32 v5, v4
	v_lshrrev_b32_e32 v4, s63, v87
	v_cmp_eq_u32_e32 vcc, v4, v15
	s_or_b64 s[76:77], s[54:55], vcc
	v_bfe_u32 v5, v87, s62, 8
	v_cndmask_b32_e64 v4, 0, 1, s[76:77]
	v_lshl_add_u32 v5, v5, 2, v3
	ds_add_u32 v5, v4
	v_lshrrev_b32_e32 v4, s63, v88
	v_cmp_eq_u32_e32 vcc, v4, v15
	s_or_b64 s[76:77], s[54:55], vcc
	v_bfe_u32 v5, v88, s62, 8
	v_cndmask_b32_e64 v4, 0, 1, s[76:77]
	v_lshl_add_u32 v5, v5, 2, v3
	ds_add_u32 v5, v4
	v_lshrrev_b32_e32 v4, s63, v89
	v_cmp_eq_u32_e32 vcc, v4, v15
	s_or_b64 s[76:77], s[54:55], vcc
	v_bfe_u32 v5, v89, s62, 8
	v_cndmask_b32_e64 v4, 0, 1, s[76:77]
	v_lshl_add_u32 v5, v5, 2, v3
	ds_add_u32 v5, v4
	v_lshrrev_b32_e32 v4, s63, v90
	v_cmp_eq_u32_e32 vcc, v4, v15
	s_or_b64 s[76:77], s[54:55], vcc
	v_bfe_u32 v5, v90, s62, 8
	v_cndmask_b32_e64 v4, 0, 1, s[76:77]
	v_lshl_add_u32 v5, v5, 2, v3
	ds_add_u32 v5, v4
	v_lshrrev_b32_e32 v4, s63, v91
	v_cmp_eq_u32_e32 vcc, v4, v15
	s_or_b64 s[76:77], s[54:55], vcc
	v_bfe_u32 v5, v91, s62, 8
	v_cndmask_b32_e64 v4, 0, 1, s[76:77]
	v_lshl_add_u32 v5, v5, 2, v3
	ds_add_u32 v5, v4
	v_lshrrev_b32_e32 v4, s63, v92
	v_cmp_eq_u32_e32 vcc, v4, v15
	s_or_b64 s[76:77], s[54:55], vcc
	v_bfe_u32 v5, v92, s62, 8
	v_cndmask_b32_e64 v4, 0, 1, s[76:77]
	v_lshl_add_u32 v5, v5, 2, v3
	ds_add_u32 v5, v4
	v_lshrrev_b32_e32 v4, s63, v93
	v_cmp_eq_u32_e32 vcc, v4, v15
	s_or_b64 s[76:77], s[54:55], vcc
	v_bfe_u32 v5, v93, s62, 8
	v_cndmask_b32_e64 v4, 0, 1, s[76:77]
	v_lshl_add_u32 v5, v5, 2, v3
	ds_add_u32 v5, v4
; #define LAS __attribute__((address_space(3)))
; __global__ void __launch_bounds__(NWAVES * 64, 2) mega_fwd(Args args) {
;     ...
;             for (int pass = 0; pass < 4; ++pass) { const int shift = 24 - 8 * pass;
;                 LAS unsigned* qst = (LAS unsigned*)(F.lds + 40960 + (pass & 1) * 512); LAS unsigned* qstn = (LAS unsigned*)(F.lds + 40960 + ((pass & 1) ^ 1) * 512);
;                 for (int i2 = tid; i2 < 32 * HSTR; i2 += 512) hist[i2] = 0u;
;                 __syncthreads();
;                 if (pass > 0) prefix = qst[2 * r32];
;                 const int pshift = (pass == 0) ? 31 : shift + 8; const unsigned pmask = (pass == 0) ? 0u : 0xffffffffu;
; #pragma unroll
;                 for (int ti = 0; ti < 4; ++ti)
; #pragma unroll
;                     for (int e = 0; e < 32; ++e) { const unsigned k = keys[ti][e];
;                         const unsigned x = ((k >> pshift) ^ prefix) & pmask; const unsigned inc = 1u - __builtin_elementwise_min(x, 1u);
;                         if (F.wave + 8 * ti < ntiles) __hip_atomic_fetch_add(hist + r32 * HSTR + ((k >> shift) & 255u), inc, __ATOMIC_RELAXED, __HIP_MEMORY_SCOPE_WORKGROUP);
;                         if ((e & 7) == 7) __builtin_amdgcn_sched_barrier(0); }
.LBB0_687:
	s_and_b64 vcc, exec, s[34:35]
	s_cbranch_vccnz .LBB0_689
	s_and_b64 vcc, exec, s[78:79]
	s_cbranch_vccz .Lrx_slow_g10
	v_xor_b32_e32 v172, v181, v170
	v_xor_b32_e32 v173, v181, v167
	v_xor_b32_e32 v174, v181, v169
	v_xor_b32_e32 v175, v181, v165
	v_xor_b32_e32 v176, v181, v166
	v_xor_b32_e32 v177, v181, v168
	v_xor_b32_e32 v178, v181, v164
	v_xor_b32_e32 v179, v181, v162
	v_min3_u32 v172, v172, v173, v174
	v_min3_u32 v175, v175, v176, v177
	v_min3_u32 v172, v172, v175, v178
	v_min_u32_e32 v172, v172, v179
	v_cmp_gt_u32_e32 vcc, s92, v172
	s_cbranch_vccz .LBB0_689
.Lrx_slow_g10:
	v_lshrrev_b32_e32 v4, s63, v170
	s_waitcnt lgkmcnt(0)
	v_cmp_eq_u32_e32 vcc, v4, v15
	s_or_b64 s[76:77], s[54:55], vcc
	v_bfe_u32 v5, v170, s62, 8
	v_cndmask_b32_e64 v4, 0, 1, s[76:77]
	v_lshl_add_u32 v5, v5, 2, v3
	ds_add_u32 v5, v4
	v_lshrrev_b32_e32 v4, s63, v167
	v_cmp_eq_u32_e32 vcc, v4, v15
	s_or_b64 s[76:77], s[54:55], vcc
	v_bfe_u32 v5, v167, s62, 8
	v_cndmask_b32_e64 v4, 0, 1, s[76:77]
	v_lshl_add_u32 v5, v5, 2, v3
	ds_add_u32 v5, v4
	v_lshrrev_b32_e32 v4, s63, v169
	v_cmp_eq_u32_e32 vcc, v4, v15
	s_or_b64 s[76:77], s[54:55], vcc
	v_bfe_u32 v5, v169, s62, 8
	v_cndmask_b32_e64 v4, 0, 1, s[76:77]
	v_lshl_add_u32 v5, v5, 2, v3
	ds_add_u32 v5, v4
	v_lshrrev_b32_e32 v4, s63, v165
	v_cmp_eq_u32_e32 vcc, v4, v15
	s_or_b64 s[76:77], s[54:55], vcc
	v_bfe_u32 v5, v165, s62, 8
	v_cndmask_b32_e64 v4, 0, 1, s[76:77]
	v_lshl_add_u32 v5, v5, 2, v3
	ds_add_u32 v5, v4
	v_lshrrev_b32_e32 v4, s63, v166
	v_cmp_eq_u32_e32 vcc, v4, v15
	s_or_b64 s[76:77], s[54:55], vcc
	v_bfe_u32 v5, v166, s62, 8
	v_cndmask_b32_e64 v4, 0, 1, s[76:77]
	v_lshl_add_u32 v5, v5, 2, v3
	ds_add_u32 v5, v4
	v_lshrrev_b32_e32 v4, s63, v168
	v_cmp_eq_u32_e32 vcc, v4, v15
	s_or_b64 s[76:77], s[54:55], vcc
	v_bfe_u32 v5, v168, s62, 8
	v_cndmask_b32_e64 v4, 0, 1, s[76:77]
	v_lshl_add_u32 v5, v5, 2, v3
	ds_add_u32 v5, v4
	v_lshrrev_b32_e32 v4, s63, v164
	v_cmp_eq_u32_e32 vcc, v4, v15
	s_or_b64 s[76:77], s[54:55], vcc
	v_bfe_u32 v5, v164, s62, 8
	v_cndmask_b32_e64 v4, 0, 1, s[76:77]
	v_lshl_add_u32 v5, v5, 2, v3
	ds_add_u32 v5, v4
	v_lshrrev_b32_e32 v4, s63, v162
	v_cmp_eq_u32_e32 vcc, v4, v15
	s_or_b64 s[76:77], s[54:55], vcc
	v_bfe_u32 v5, v162, s62, 8
	v_cndmask_b32_e64 v4, 0, 1, s[76:77]
	v_lshl_add_u32 v5, v5, 2, v3
	ds_add_u32 v5, v4
.LBB0_689:
	s_and_b64 vcc, exec, s[34:35]
	s_cbranch_vccnz .LBB0_691
	s_and_b64 vcc, exec, s[78:79]
	s_cbranch_vccz .Lrx_slow_g11
	v_xor_b32_e32 v172, v181, v163
	v_xor_b32_e32 v173, v181, v158
	v_xor_b32_e32 v174, v181, v157
	v_xor_b32_e32 v175, v181, v160
	v_xor_b32_e32 v176, v181, v161
	v_xor_b32_e32 v177, v181, v159
	v_xor_b32_e32 v178, v181, v95
	v_xor_b32_e32 v179, v181, v64
	v_min3_u32 v172, v172, v173, v174
	v_min3_u32 v175, v175, v176, v177
	v_min3_u32 v172, v172, v175, v178
	v_min_u32_e32 v172, v172, v179
	v_cmp_gt_u32_e32 vcc, s92, v172
	s_cbranch_vccz .LBB0_691
.Lrx_slow_g11:
	v_lshrrev_b32_e32 v4, s63, v163
	s_waitcnt lgkmcnt(0)
	v_cmp_eq_u32_e32 vcc, v4, v15
	s_or_b64 s[76:77], s[54:55], vcc
	v_bfe_u32 v5, v163, s62, 8
	v_cndmask_b32_e64 v4, 0, 1, s[76:77]
	v_lshl_add_u32 v5, v5, 2, v3
	ds_add_u32 v5, v4
	v_lshrrev_b32_e32 v4, s63, v158
	v_cmp_eq_u32_e32 vcc, v4, v15
	s_or_b64 s[76:77], s[54:55], vcc
	v_bfe_u32 v5, v158, s62, 8
	v_cndmask_b32_e64 v4, 0, 1, s[76:77]
	v_lshl_add_u32 v5, v5, 2, v3
	ds_add_u32 v5, v4
	v_lshrrev_b32_e32 v4, s63, v157
	v_cmp_eq_u32_e32 vcc, v4, v15
	s_or_b64 s[76:77], s[54:55], vcc
	v_bfe_u32 v5, v157, s62, 8
	v_cndmask_b32_e64 v4, 0, 1, s[76:77]
	v_lshl_add_u32 v5, v5, 2, v3
	ds_add_u32 v5, v4
	v_lshrrev_b32_e32 v4, s63, v160
	v_cmp_eq_u32_e32 vcc, v4, v15
	s_or_b64 s[76:77], s[54:55], vcc
	v_bfe_u32 v5, v160, s62, 8
	v_cndmask_b32_e64 v4, 0, 1, s[76:77]
	v_lshl_add_u32 v5, v5, 2, v3
	ds_add_u32 v5, v4
	v_lshrrev_b32_e32 v4, s63, v161
	v_cmp_eq_u32_e32 vcc, v4, v15
	s_or_b64 s[76:77], s[54:55], vcc
	v_bfe_u32 v5, v161, s62, 8
	v_cndmask_b32_e64 v4, 0, 1, s[76:77]
	v_lshl_add_u32 v5, v5, 2, v3
	ds_add_u32 v5, v4
	v_lshrrev_b32_e32 v4, s63, v159
	v_cmp_eq_u32_e32 vcc, v4, v15
	s_or_b64 s[76:77], s[54:55], vcc
	v_bfe_u32 v5, v159, s62, 8
	v_cndmask_b32_e64 v4, 0, 1, s[76:77]
	v_lshl_add_u32 v5, v5, 2, v3
	ds_add_u32 v5, v4
	v_lshrrev_b32_e32 v4, s63, v95
	v_cmp_eq_u32_e32 vcc, v4, v15
	s_or_b64 s[76:77], s[54:55], vcc
	v_bfe_u32 v5, v95, s62, 8
	v_cndmask_b32_e64 v4, 0, 1, s[76:77]
	v_lshl_add_u32 v5, v5, 2, v3
	ds_add_u32 v5, v4
	v_lshrrev_b32_e32 v4, s63, v64
	v_cmp_eq_u32_e32 vcc, v4, v15
	s_or_b64 s[76:77], s[54:55], vcc
	v_bfe_u32 v5, v64, s62, 8
	v_cndmask_b32_e64 v4, 0, 1, s[76:77]
	v_lshl_add_u32 v5, v5, 2, v3
	ds_add_u32 v5, v4
.LBB0_691:
	s_and_b64 vcc, exec, s[30:31]
	s_cbranch_vccnz .LBB0_693
	s_and_b64 vcc, exec, s[78:79]
	s_cbranch_vccz .Lrx_slow_g12
	v_xor_b32_e32 v172, v181, v105
	v_xor_b32_e32 v173, v181, v106
	v_xor_b32_e32 v174, v181, v104
	v_xor_b32_e32 v175, v181, v107
	v_xor_b32_e32 v176, v181, v66
	v_xor_b32_e32 v177, v181, v67
	v_xor_b32_e32 v178, v181, v68
	v_xor_b32_e32 v179, v181, v69
	v_min3_u32 v172, v172, v173, v174
	v_min3_u32 v175, v175, v176, v177
	v_min3_u32 v172, v172, v175, v178
	v_min_u32_e32 v172, v172, v179
	v_cmp_gt_u32_e32 vcc, s92, v172
	s_cbranch_vccz .LBB0_693
; #define LAS __attribute__((address_space(3)))
; __global__ void __launch_bounds__(NWAVES * 64, 2) mega_fwd(Args args) {
;     ...
;             for (int pass = 0; pass < 4; ++pass) { const int shift = 24 - 8 * pass;
;                 LAS unsigned* qst = (LAS unsigned*)(F.lds + 40960 + (pass & 1) * 512); LAS unsigned* qstn = (LAS unsigned*)(F.lds + 40960 + ((pass & 1) ^ 1) * 512);
;                 for (int i2 = tid; i2 < 32 * HSTR; i2 += 512) hist[i2] = 0u;
;                 __syncthreads();
;                 if (pass > 0) prefix = qst[2 * r32];
;                 const int pshift = (pass == 0) ? 31 : shift + 8; const unsigned pmask = (pass == 0) ? 0u : 0xffffffffu;
; #pragma unroll
;                 for (int ti = 0; ti < 4; ++ti)
; #pragma unroll
;                     for (int e = 0; e < 32; ++e) { const unsigned k = keys[ti][e];
;                         const unsigned x = ((k >> pshift) ^ prefix) & pmask; const unsigned inc = 1u - __builtin_elementwise_min(x, 1u);
;                         if (F.wave + 8 * ti < ntiles) __hip_atomic_fetch_add(hist + r32 * HSTR + ((k >> shift) & 255u), inc, __ATOMIC_RELAXED, __HIP_MEMORY_SCOPE_WORKGROUP);
;                         if ((e & 7) == 7) __builtin_amdgcn_sched_barrier(0); }
.Lrx_slow_g12:
	v_lshrrev_b32_e32 v4, s63, v105
	s_waitcnt lgkmcnt(0)
	v_cmp_eq_u32_e32 vcc, v4, v15
	s_or_b64 s[76:77], s[54:55], vcc
	v_bfe_u32 v5, v105, s62, 8
	v_cndmask_b32_e64 v4, 0, 1, s[76:77]
	v_lshl_add_u32 v5, v5, 2, v3
	ds_add_u32 v5, v4
	v_lshrrev_b32_e32 v4, s63, v106
	v_cmp_eq_u32_e32 vcc, v4, v15
	s_or_b64 s[76:77], s[54:55], vcc
	v_bfe_u32 v5, v106, s62, 8
	v_cndmask_b32_e64 v4, 0, 1, s[76:77]
	v_lshl_add_u32 v5, v5, 2, v3
	ds_add_u32 v5, v4
	v_lshrrev_b32_e32 v4, s63, v104
	v_cmp_eq_u32_e32 vcc, v4, v15
	s_or_b64 s[76:77], s[54:55], vcc
	v_bfe_u32 v5, v104, s62, 8
	v_cndmask_b32_e64 v4, 0, 1, s[76:77]
	v_lshl_add_u32 v5, v5, 2, v3
	ds_add_u32 v5, v4
	v_lshrrev_b32_e32 v4, s63, v107
	v_cmp_eq_u32_e32 vcc, v4, v15
	s_or_b64 s[76:77], s[54:55], vcc
	v_bfe_u32 v5, v107, s62, 8
	v_cndmask_b32_e64 v4, 0, 1, s[76:77]
	v_lshl_add_u32 v5, v5, 2, v3
	ds_add_u32 v5, v4
	v_lshrrev_b32_e32 v4, s63, v66
	v_cmp_eq_u32_e32 vcc, v4, v15
	s_or_b64 s[76:77], s[54:55], vcc
	v_bfe_u32 v5, v66, s62, 8
	v_cndmask_b32_e64 v4, 0, 1, s[76:77]
	v_lshl_add_u32 v5, v5, 2, v3
	ds_add_u32 v5, v4
	v_lshrrev_b32_e32 v4, s63, v67
	v_cmp_eq_u32_e32 vcc, v4, v15
	s_or_b64 s[76:77], s[54:55], vcc
	v_bfe_u32 v5, v67, s62, 8
	v_cndmask_b32_e64 v4, 0, 1, s[76:77]
	v_lshl_add_u32 v5, v5, 2, v3
	ds_add_u32 v5, v4
	v_lshrrev_b32_e32 v4, s63, v68
	v_cmp_eq_u32_e32 vcc, v4, v15
	s_or_b64 s[76:77], s[54:55], vcc
	v_bfe_u32 v5, v68, s62, 8
	v_cndmask_b32_e64 v4, 0, 1, s[76:77]
	v_lshl_add_u32 v5, v5, 2, v3
	ds_add_u32 v5, v4
	v_lshrrev_b32_e32 v4, s63, v69
	v_cmp_eq_u32_e32 vcc, v4, v15
	s_or_b64 s[76:77], s[54:55], vcc
	v_bfe_u32 v5, v69, s62, 8
	v_cndmask_b32_e64 v4, 0, 1, s[76:77]
	v_lshl_add_u32 v5, v5, 2, v3
	ds_add_u32 v5, v4
.LBB0_693:
	s_and_b64 vcc, exec, s[30:31]
	s_cbranch_vccnz .LBB0_695
	s_and_b64 vcc, exec, s[78:79]
	s_cbranch_vccz .Lrx_slow_g13
	v_xor_b32_e32 v172, v181, v54
	v_xor_b32_e32 v173, v181, v55
	v_xor_b32_e32 v174, v181, v56
	v_xor_b32_e32 v175, v181, v57
	v_xor_b32_e32 v176, v181, v58
	v_xor_b32_e32 v177, v181, v59
	v_xor_b32_e32 v178, v181, v60
	v_xor_b32_e32 v179, v181, v61
	v_min3_u32 v172, v172, v173, v174
	v_min3_u32 v175, v175, v176, v177
	v_min3_u32 v172, v172, v175, v178
	v_min_u32_e32 v172, v172, v179
	v_cmp_gt_u32_e32 vcc, s92, v172
	s_cbranch_vccz .LBB0_695
.Lrx_slow_g13:
	v_lshrrev_b32_e32 v4, s63, v54
	s_waitcnt lgkmcnt(0)
	v_cmp_eq_u32_e32 vcc, v4, v15
	s_or_b64 s[76:77], s[54:55], vcc
	v_bfe_u32 v5, v54, s62, 8
	v_cndmask_b32_e64 v4, 0, 1, s[76:77]
	v_lshl_add_u32 v5, v5, 2, v3
	ds_add_u32 v5, v4
	v_lshrrev_b32_e32 v4, s63, v55
	v_cmp_eq_u32_e32 vcc, v4, v15
	s_or_b64 s[76:77], s[54:55], vcc
	v_bfe_u32 v5, v55, s62, 8
	v_cndmask_b32_e64 v4, 0, 1, s[76:77]
	v_lshl_add_u32 v5, v5, 2, v3
	ds_add_u32 v5, v4
	v_lshrrev_b32_e32 v4, s63, v56
	v_cmp_eq_u32_e32 vcc, v4, v15
	s_or_b64 s[76:77], s[54:55], vcc
	v_bfe_u32 v5, v56, s62, 8
	v_cndmask_b32_e64 v4, 0, 1, s[76:77]
	v_lshl_add_u32 v5, v5, 2, v3
	ds_add_u32 v5, v4
	v_lshrrev_b32_e32 v4, s63, v57
	v_cmp_eq_u32_e32 vcc, v4, v15
	s_or_b64 s[76:77], s[54:55], vcc
	v_bfe_u32 v5, v57, s62, 8
	v_cndmask_b32_e64 v4, 0, 1, s[76:77]
	v_lshl_add_u32 v5, v5, 2, v3
	ds_add_u32 v5, v4
	v_lshrrev_b32_e32 v4, s63, v58
	v_cmp_eq_u32_e32 vcc, v4, v15
	s_or_b64 s[76:77], s[54:55], vcc
	v_bfe_u32 v5, v58, s62, 8
	v_cndmask_b32_e64 v4, 0, 1, s[76:77]
	v_lshl_add_u32 v5, v5, 2, v3
	ds_add_u32 v5, v4
	v_lshrrev_b32_e32 v4, s63, v59
	v_cmp_eq_u32_e32 vcc, v4, v15
	s_or_b64 s[76:77], s[54:55], vcc
	v_bfe_u32 v5, v59, s62, 8
	v_cndmask_b32_e64 v4, 0, 1, s[76:77]
	v_lshl_add_u32 v5, v5, 2, v3
	ds_add_u32 v5, v4
	v_lshrrev_b32_e32 v4, s63, v60
	v_cmp_eq_u32_e32 vcc, v4, v15
	s_or_b64 s[76:77], s[54:55], vcc
	v_bfe_u32 v5, v60, s62, 8
	v_cndmask_b32_e64 v4, 0, 1, s[76:77]
	v_lshl_add_u32 v5, v5, 2, v3
	ds_add_u32 v5, v4
	v_lshrrev_b32_e32 v4, s63, v61
	v_cmp_eq_u32_e32 vcc, v4, v15
	s_or_b64 s[76:77], s[54:55], vcc
	v_bfe_u32 v5, v61, s62, 8
	v_cndmask_b32_e64 v4, 0, 1, s[76:77]
	v_lshl_add_u32 v5, v5, 2, v3
	ds_add_u32 v5, v4
; #define LAS __attribute__((address_space(3)))
; __global__ void __launch_bounds__(NWAVES * 64, 2) mega_fwd(Args args) {
;     ...
;             for (int pass = 0; pass < 4; ++pass) { const int shift = 24 - 8 * pass;
;                 LAS unsigned* qst = (LAS unsigned*)(F.lds + 40960 + (pass & 1) * 512); LAS unsigned* qstn = (LAS unsigned*)(F.lds + 40960 + ((pass & 1) ^ 1) * 512);
;                 for (int i2 = tid; i2 < 32 * HSTR; i2 += 512) hist[i2] = 0u;
;                 __syncthreads();
;                 if (pass > 0) prefix = qst[2 * r32];
;                 const int pshift = (pass == 0) ? 31 : shift + 8; const unsigned pmask = (pass == 0) ? 0u : 0xffffffffu;
; #pragma unroll
;                 for (int ti = 0; ti < 4; ++ti)
; #pragma unroll
;                     for (int e = 0; e < 32; ++e) { const unsigned k = keys[ti][e];
;                         const unsigned x = ((k >> pshift) ^ prefix) & pmask; const unsigned inc = 1u - __builtin_elementwise_min(x, 1u);
;                         if (F.wave + 8 * ti < ntiles) __hip_atomic_fetch_add(hist + r32 * HSTR + ((k >> shift) & 255u), inc, __ATOMIC_RELAXED, __HIP_MEMORY_SCOPE_WORKGROUP);
;                         if ((e & 7) == 7) __builtin_amdgcn_sched_barrier(0); }
.LBB0_695:
	s_and_b64 vcc, exec, s[30:31]
	s_cbranch_vccnz .LBB0_697
	s_and_b64 vcc, exec, s[78:79]
	s_cbranch_vccz .Lrx_slow_g14
	v_xor_b32_e32 v172, v181, v26
	v_xor_b32_e32 v173, v181, v23
	v_xor_b32_e32 v174, v181, v25
	v_xor_b32_e32 v175, v181, v21
	v_xor_b32_e32 v176, v181, v22
	v_xor_b32_e32 v177, v181, v24
	v_xor_b32_e32 v178, v181, v20
	v_xor_b32_e32 v179, v181, v18
	v_min3_u32 v172, v172, v173, v174
	v_min3_u32 v175, v175, v176, v177
	v_min3_u32 v172, v172, v175, v178
	v_min_u32_e32 v172, v172, v179
	v_cmp_gt_u32_e32 vcc, s92, v172
	s_cbranch_vccz .LBB0_697
.Lrx_slow_g14:
	v_lshrrev_b32_e32 v4, s63, v26
	s_waitcnt lgkmcnt(0)
	v_cmp_eq_u32_e32 vcc, v4, v15
	s_or_b64 s[76:77], s[54:55], vcc
	v_bfe_u32 v5, v26, s62, 8
	v_cndmask_b32_e64 v4, 0, 1, s[76:77]
	v_lshl_add_u32 v5, v5, 2, v3
	ds_add_u32 v5, v4
	v_lshrrev_b32_e32 v4, s63, v23
	v_cmp_eq_u32_e32 vcc, v4, v15
	s_or_b64 s[76:77], s[54:55], vcc
	v_bfe_u32 v5, v23, s62, 8
	v_cndmask_b32_e64 v4, 0, 1, s[76:77]
	v_lshl_add_u32 v5, v5, 2, v3
	ds_add_u32 v5, v4
	v_lshrrev_b32_e32 v4, s63, v25
	v_cmp_eq_u32_e32 vcc, v4, v15
	s_or_b64 s[76:77], s[54:55], vcc
	v_bfe_u32 v5, v25, s62, 8
	v_cndmask_b32_e64 v4, 0, 1, s[76:77]
	v_lshl_add_u32 v5, v5, 2, v3
	ds_add_u32 v5, v4
	v_lshrrev_b32_e32 v4, s63, v21
	v_cmp_eq_u32_e32 vcc, v4, v15
	s_or_b64 s[76:77], s[54:55], vcc
	v_bfe_u32 v5, v21, s62, 8
	v_cndmask_b32_e64 v4, 0, 1, s[76:77]
	v_lshl_add_u32 v5, v5, 2, v3
	ds_add_u32 v5, v4
	v_lshrrev_b32_e32 v4, s63, v22
	v_cmp_eq_u32_e32 vcc, v4, v15
	s_or_b64 s[76:77], s[54:55], vcc
	v_bfe_u32 v5, v22, s62, 8
	v_cndmask_b32_e64 v4, 0, 1, s[76:77]
	v_lshl_add_u32 v5, v5, 2, v3
	ds_add_u32 v5, v4
	v_lshrrev_b32_e32 v4, s63, v24
	v_cmp_eq_u32_e32 vcc, v4, v15
	s_or_b64 s[76:77], s[54:55], vcc
	v_bfe_u32 v5, v24, s62, 8
	v_cndmask_b32_e64 v4, 0, 1, s[76:77]
	v_lshl_add_u32 v5, v5, 2, v3
	ds_add_u32 v5, v4
	v_lshrrev_b32_e32 v4, s63, v20
	v_cmp_eq_u32_e32 vcc, v4, v15
	s_or_b64 s[76:77], s[54:55], vcc
	v_bfe_u32 v5, v20, s62, 8
	v_cndmask_b32_e64 v4, 0, 1, s[76:77]
	v_lshl_add_u32 v5, v5, 2, v3
	ds_add_u32 v5, v4
	v_lshrrev_b32_e32 v4, s63, v18
	v_cmp_eq_u32_e32 vcc, v4, v15
	s_or_b64 s[76:77], s[54:55], vcc
	v_bfe_u32 v5, v18, s62, 8
	v_cndmask_b32_e64 v4, 0, 1, s[76:77]
	v_lshl_add_u32 v5, v5, 2, v3
	ds_add_u32 v5, v4
.LBB0_697:
	s_and_b64 vcc, exec, s[30:31]
	s_cbranch_vccnz .LBB0_699
	s_and_b64 vcc, exec, s[78:79]
	s_cbranch_vccz .Lrx_slow_g15
	v_xor_b32_e32 v172, v181, v19
	v_xor_b32_e32 v173, v181, v11
	v_xor_b32_e32 v174, v181, v9
	v_xor_b32_e32 v175, v181, v13
	v_xor_b32_e32 v176, v181, v12
	v_xor_b32_e32 v177, v181, v10
	v_xor_b32_e32 v178, v181, v8
	v_xor_b32_e32 v179, v181, v2
	v_min3_u32 v172, v172, v173, v174
	v_min3_u32 v175, v175, v176, v177
	v_min3_u32 v172, v172, v175, v178
	v_min_u32_e32 v172, v172, v179
	v_cmp_gt_u32_e32 vcc, s92, v172
	s_cbranch_vccz .LBB0_699
.Lrx_slow_g15:
	v_lshrrev_b32_e32 v4, s63, v19
	s_waitcnt lgkmcnt(0)
	v_cmp_eq_u32_e32 vcc, v4, v15
	s_or_b64 s[76:77], s[54:55], vcc
	v_bfe_u32 v5, v19, s62, 8
	v_cndmask_b32_e64 v4, 0, 1, s[76:77]
	v_lshl_add_u32 v5, v5, 2, v3
	ds_add_u32 v5, v4
	v_lshrrev_b32_e32 v4, s63, v11
	v_cmp_eq_u32_e32 vcc, v4, v15
	s_or_b64 s[76:77], s[54:55], vcc
	v_bfe_u32 v5, v11, s62, 8
	v_cndmask_b32_e64 v4, 0, 1, s[76:77]
	v_lshl_add_u32 v5, v5, 2, v3
	ds_add_u32 v5, v4
	v_lshrrev_b32_e32 v4, s63, v9
	v_cmp_eq_u32_e32 vcc, v4, v15
	s_or_b64 s[76:77], s[54:55], vcc
	v_bfe_u32 v5, v9, s62, 8
	v_cndmask_b32_e64 v4, 0, 1, s[76:77]
	v_lshl_add_u32 v5, v5, 2, v3
	ds_add_u32 v5, v4
	v_lshrrev_b32_e32 v4, s63, v13
	v_cmp_eq_u32_e32 vcc, v4, v15
	s_or_b64 s[76:77], s[54:55], vcc
	v_bfe_u32 v5, v13, s62, 8
	v_cndmask_b32_e64 v4, 0, 1, s[76:77]
	v_lshl_add_u32 v5, v5, 2, v3
	ds_add_u32 v5, v4
	v_lshrrev_b32_e32 v4, s63, v12
	v_cmp_eq_u32_e32 vcc, v4, v15
	s_or_b64 s[76:77], s[54:55], vcc
	v_bfe_u32 v5, v12, s62, 8
	v_cndmask_b32_e64 v4, 0, 1, s[76:77]
	v_lshl_add_u32 v5, v5, 2, v3
	ds_add_u32 v5, v4
	v_lshrrev_b32_e32 v4, s63, v10
	v_cmp_eq_u32_e32 vcc, v4, v15
	s_or_b64 s[76:77], s[54:55], vcc
	v_bfe_u32 v5, v10, s62, 8
	v_cndmask_b32_e64 v4, 0, 1, s[76:77]
	v_lshl_add_u32 v5, v5, 2, v3
	ds_add_u32 v5, v4
	v_lshrrev_b32_e32 v4, s63, v8
	v_cmp_eq_u32_e32 vcc, v4, v15
	s_or_b64 s[76:77], s[54:55], vcc
	v_bfe_u32 v5, v8, s62, 8
	v_cndmask_b32_e64 v4, 0, 1, s[76:77]
	v_lshl_add_u32 v5, v5, 2, v3
	ds_add_u32 v5, v4
	v_lshrrev_b32_e32 v4, s63, v2
	v_cmp_eq_u32_e32 vcc, v4, v15
	s_or_b64 s[54:55], s[54:55], vcc
	v_bfe_u32 v5, v2, s62, 8
	v_cndmask_b32_e64 v4, 0, 1, s[54:55]
	v_lshl_add_u32 v5, v5, 2, v3
	ds_add_u32 v5, v4
